# speedup vs baseline: 1.0003x; 1.0003x over previous
.LBB1_1:
	s_and_b32 s0, s29, 0x10000
	v_add_u32_e32 v211, s0, v209
	v_add_u32_e32 v242, s0, v210
	ds_read_b128 v[212:215], v242 offset:0
	ds_read_b128 v[216:219], v242 offset:2048
	ds_read_b128 v[220:223], v242 offset:4096
	ds_read_b128 v[224:227], v242 offset:6144
	ds_read_b128 v[228:231], v211 offset:0
	ds_read_b128 v[232:235], v211 offset:2048
	ds_read_b128 v[236:239], v211 offset:4096
	ds_read_b128 v[244:247], v211 offset:6144
	ds_read_b128 v[248:251], v211 offset:8192
	ds_read_b128 v[252:255], v211 offset:10240
	s_waitcnt lgkmcnt(4)
	v_mfma_f32_16x16x32_bf16 v[174:177], v[212:215], v[228:231], v[174:177]
	v_mfma_f32_16x16x32_bf16 v[170:173], v[216:219], v[228:231], v[170:173]
	v_mfma_f32_16x16x32_bf16 v[166:169], v[220:223], v[228:231], v[166:169]
	v_mfma_f32_16x16x32_bf16 v[162:165], v[224:227], v[228:231], v[162:165]
	v_mfma_f32_16x16x32_bf16 v[158:161], v[212:215], v[232:235], v[158:161]
	v_mfma_f32_16x16x32_bf16 v[154:157], v[216:219], v[232:235], v[154:157]
	v_mfma_f32_16x16x32_bf16 v[150:153], v[220:223], v[232:235], v[150:153]
	v_mfma_f32_16x16x32_bf16 v[146:149], v[224:227], v[232:235], v[146:149]
	ds_read_b128 v[228:231], v211 offset:12288
	ds_read_b128 v[232:235], v211 offset:14336
	s_waitcnt lgkmcnt(4)
	v_mfma_f32_16x16x32_bf16 v[142:145], v[212:215], v[236:239], v[142:145]
	v_mfma_f32_16x16x32_bf16 v[138:141], v[216:219], v[236:239], v[138:141]
	v_mfma_f32_16x16x32_bf16 v[134:137], v[220:223], v[236:239], v[134:137]
	v_mfma_f32_16x16x32_bf16 v[130:133], v[224:227], v[236:239], v[130:133]
	v_mfma_f32_16x16x32_bf16 v[126:129], v[212:215], v[244:247], v[126:129]
	v_mfma_f32_16x16x32_bf16 v[122:125], v[216:219], v[244:247], v[122:125]
	v_mfma_f32_16x16x32_bf16 v[118:121], v[220:223], v[244:247], v[118:121]
	v_mfma_f32_16x16x32_bf16 v[114:117], v[224:227], v[244:247], v[114:117]
	s_waitcnt lgkmcnt(2)
	v_mfma_f32_16x16x32_bf16 v[110:113], v[212:215], v[248:251], v[110:113]
	v_mfma_f32_16x16x32_bf16 v[106:109], v[216:219], v[248:251], v[106:109]
	v_mfma_f32_16x16x32_bf16 v[102:105], v[220:223], v[248:251], v[102:105]
	v_mfma_f32_16x16x32_bf16 v[98:101], v[224:227], v[248:251], v[98:101]
	v_mfma_f32_16x16x32_bf16 v[94:97], v[212:215], v[252:255], v[94:97]
	v_mfma_f32_16x16x32_bf16 v[90:93], v[216:219], v[252:255], v[90:93]
	v_mfma_f32_16x16x32_bf16 v[86:89], v[220:223], v[252:255], v[86:89]
	v_mfma_f32_16x16x32_bf16 v[82:85], v[224:227], v[252:255], v[82:85]
	s_waitcnt lgkmcnt(0)
	v_mfma_f32_16x16x32_bf16 v[78:81], v[212:215], v[228:231], v[78:81]
	v_mfma_f32_16x16x32_bf16 v[74:77], v[216:219], v[228:231], v[74:77]
	v_mfma_f32_16x16x32_bf16 v[70:73], v[220:223], v[228:231], v[70:73]
	v_mfma_f32_16x16x32_bf16 v[66:69], v[224:227], v[228:231], v[66:69]
	v_mfma_f32_16x16x32_bf16 v[62:65], v[212:215], v[232:235], v[62:65]
	v_mfma_f32_16x16x32_bf16 v[58:61], v[216:219], v[232:235], v[58:61]
	v_mfma_f32_16x16x32_bf16 v[54:57], v[220:223], v[232:235], v[54:57]
	v_mfma_f32_16x16x32_bf16 v[50:53], v[224:227], v[232:235], v[50:53]
	s_xor_b32 s0, s0, 0x10000
	s_and_b32 s1, s22, 0x3c0
	s_add_i32 s23, s0, 0
	s_lshl_b32 s0, s1, 2
	s_add_u32 s20, s25, s0
	s_waitcnt vmcnt(10)
	v_cvt_pk_bf16_f32 v46, v46, v47
	v_cvt_pk_bf16_f32 v47, v48, v49
	v_cvt_pk_bf16_f32 v48, v42, v43
	v_cvt_pk_bf16_f32 v49, v44, v45
	s_waitcnt vmcnt(8)
	v_cvt_pk_bf16_f32 v38, v38, v39
	v_cvt_pk_bf16_f32 v39, v40, v41
	v_cvt_pk_bf16_f32 v40, v34, v35
	v_add_u32_e32 v34, s23, v208
	s_addc_u32 s21, s26, 0
	s_lshl_b32 s0, s1, 1
	v_cvt_pk_bf16_f32 v41, v36, v37
	v_lshlrev_b32_e32 v182, 2, v178
	v_add_u32_e32 v35, s23, v205
	v_add_u32_e32 v36, s23, v206
	v_add_u32_e32 v37, s23, v207
	ds_write_b128 v34, v[46:49]
	ds_write_b128 v35, v[38:41]
	s_waitcnt vmcnt(7)
	ds_write_b128 v36, v[30:33] offset:32768
	s_waitcnt vmcnt(6)
	ds_write_b128 v37, v[26:29] offset:32768
	v_lshl_add_u64 v[26:27], s[20:21], 0, v[180:181]
	v_lshl_add_u64 v[28:29], s[20:21], 0, v[184:185]
	s_add_u32 s0, s27, s0
	v_lshl_add_u64 v[26:27], v[26:27], 0, v[182:183]
	v_lshl_add_u64 v[28:29], v[28:29], 0, v[182:183]
	s_addc_u32 s1, s28, 0
	v_lshlrev_b32_e32 v240, 1, v178
	v_mov_b32_e32 v241, v183
	global_load_dwordx4 v[42:45], v[26:27], off offset:16
	global_load_dwordx4 v[46:49], v[26:27], off
	global_load_dwordx4 v[34:37], v[28:29], off offset:16
	global_load_dwordx4 v[38:41], v[28:29], off
	v_lshl_add_u64 v[26:27], s[0:1], 0, v[186:187]
	v_lshl_add_u64 v[28:29], s[0:1], 0, v[188:189]
	v_lshl_add_u64 v[26:27], v[26:27], 0, v[240:241]
	v_lshl_add_u64 v[28:29], v[28:29], 0, v[240:241]
	global_load_dwordx4 v[30:33], v[26:27], off
	s_nop 0
	global_load_dwordx4 v[26:29], v[28:29], off
	ds_read_b128 v[212:215], v242 offset:1024
	ds_read_b128 v[216:219], v242 offset:3072
	ds_read_b128 v[220:223], v242 offset:5120
	ds_read_b128 v[224:227], v242 offset:7168
	ds_read_b128 v[228:231], v211 offset:1024
	ds_read_b128 v[232:235], v211 offset:3072
	ds_read_b128 v[236:239], v211 offset:5120
	ds_read_b128 v[244:247], v211 offset:7168
	ds_read_b128 v[248:251], v211 offset:9216
	ds_read_b128 v[252:255], v211 offset:11264
	s_waitcnt lgkmcnt(4)
	v_mfma_f32_16x16x32_bf16 v[174:177], v[212:215], v[228:231], v[174:177]
	v_mfma_f32_16x16x32_bf16 v[170:173], v[216:219], v[228:231], v[170:173]
	v_mfma_f32_16x16x32_bf16 v[166:169], v[220:223], v[228:231], v[166:169]
	v_mfma_f32_16x16x32_bf16 v[162:165], v[224:227], v[228:231], v[162:165]
	v_mfma_f32_16x16x32_bf16 v[158:161], v[212:215], v[232:235], v[158:161]
	v_mfma_f32_16x16x32_bf16 v[154:157], v[216:219], v[232:235], v[154:157]
	v_mfma_f32_16x16x32_bf16 v[150:153], v[220:223], v[232:235], v[150:153]
	v_mfma_f32_16x16x32_bf16 v[146:149], v[224:227], v[232:235], v[146:149]
	ds_read_b128 v[228:231], v211 offset:13312
	ds_read_b128 v[232:235], v211 offset:15360
	s_waitcnt lgkmcnt(4)
	v_mfma_f32_16x16x32_bf16 v[142:145], v[212:215], v[236:239], v[142:145]
	v_mfma_f32_16x16x32_bf16 v[138:141], v[216:219], v[236:239], v[138:141]
	v_mfma_f32_16x16x32_bf16 v[134:137], v[220:223], v[236:239], v[134:137]
	v_mfma_f32_16x16x32_bf16 v[130:133], v[224:227], v[236:239], v[130:133]
	v_mfma_f32_16x16x32_bf16 v[126:129], v[212:215], v[244:247], v[126:129]
	v_mfma_f32_16x16x32_bf16 v[122:125], v[216:219], v[244:247], v[122:125]
	v_mfma_f32_16x16x32_bf16 v[118:121], v[220:223], v[244:247], v[118:121]
	v_mfma_f32_16x16x32_bf16 v[114:117], v[224:227], v[244:247], v[114:117]
	s_waitcnt lgkmcnt(2)
	v_mfma_f32_16x16x32_bf16 v[110:113], v[212:215], v[248:251], v[110:113]
	v_mfma_f32_16x16x32_bf16 v[106:109], v[216:219], v[248:251], v[106:109]
	v_mfma_f32_16x16x32_bf16 v[102:105], v[220:223], v[248:251], v[102:105]
	v_mfma_f32_16x16x32_bf16 v[98:101], v[224:227], v[248:251], v[98:101]
	v_mfma_f32_16x16x32_bf16 v[94:97], v[212:215], v[252:255], v[94:97]
	v_mfma_f32_16x16x32_bf16 v[90:93], v[216:219], v[252:255], v[90:93]
	v_mfma_f32_16x16x32_bf16 v[86:89], v[220:223], v[252:255], v[86:89]
	v_mfma_f32_16x16x32_bf16 v[82:85], v[224:227], v[252:255], v[82:85]
	s_waitcnt lgkmcnt(0)
	v_mfma_f32_16x16x32_bf16 v[78:81], v[212:215], v[228:231], v[78:81]
	v_mfma_f32_16x16x32_bf16 v[74:77], v[216:219], v[228:231], v[74:77]
	v_mfma_f32_16x16x32_bf16 v[70:73], v[220:223], v[228:231], v[70:73]
	v_mfma_f32_16x16x32_bf16 v[66:69], v[224:227], v[228:231], v[66:69]
	v_mfma_f32_16x16x32_bf16 v[62:65], v[212:215], v[232:235], v[62:65]
	v_mfma_f32_16x16x32_bf16 v[58:61], v[216:219], v[232:235], v[58:61]
	v_mfma_f32_16x16x32_bf16 v[54:57], v[220:223], v[232:235], v[54:57]
	v_mfma_f32_16x16x32_bf16 v[50:53], v[224:227], v[232:235], v[50:53]
	s_waitcnt vmcnt(10)
	v_cvt_pk_bf16_f32 v22, v22, v23
	v_cvt_pk_bf16_f32 v23, v24, v25
	v_cvt_pk_bf16_f32 v24, v6, v7
	v_cvt_pk_bf16_f32 v25, v8, v9
	v_add_u32_e32 v6, s23, v204
	s_waitcnt vmcnt(9)
	v_cvt_pk_bf16_f32 v8, v2, v3
	v_add_u32_e32 v2, s23, v201
	ds_write_b128 v6, v[22:25]
	s_waitcnt vmcnt(8)
	v_cvt_pk_bf16_f32 v6, v10, v11
	v_cvt_pk_bf16_f32 v7, v12, v13
	v_cvt_pk_bf16_f32 v9, v4, v5
	ds_write_b128 v2, v[6:9]
	v_add_u32_e32 v2, s23, v202
	s_waitcnt vmcnt(7)
	ds_write_b128 v2, v[18:21] offset:32768
	v_add_u32_e32 v2, s23, v203
	s_waitcnt vmcnt(6)
	ds_write_b128 v2, v[14:17] offset:32768
	v_lshl_add_u64 v[2:3], s[20:21], 0, v[190:191]
	v_lshl_add_u64 v[2:3], v[2:3], 0, v[182:183]
	global_load_dwordx4 v[6:9], v[2:3], off offset:16
	global_load_dwordx4 v[22:25], v[2:3], off
	v_lshl_add_u64 v[2:3], s[20:21], 0, v[192:193]
	v_lshl_add_u64 v[14:15], s[0:1], 0, v[194:195]
	v_lshl_add_u64 v[16:17], s[0:1], 0, v[196:197]
	v_lshl_add_u64 v[10:11], v[2:3], 0, v[182:183]
	v_lshl_add_u64 v[14:15], v[14:15], 0, v[240:241]
	v_lshl_add_u64 v[16:17], v[16:17], 0, v[240:241]
	global_load_dwordx4 v[2:5], v[10:11], off offset:16
	s_nop 0
	global_load_dwordx4 v[10:13], v[10:11], off
	s_nop 0
	global_load_dwordx4 v[18:21], v[14:15], off
	s_nop 0
	global_load_dwordx4 v[14:17], v[16:17], off
	s_waitcnt lgkmcnt(0)
	s_add_i32 s22, s22, 64
	s_add_i32 s29, s29, 0x10000
	s_cmp_lg_u32 s29, 0xe0000
	s_barrier
	s_cbranch_scc1 .LBB1_1
	s_lshl_b64 s[0:1], s[18:19], 24
	ds_read_b128 v[180:183], v210 offset:0
	ds_read_b128 v[184:187], v210 offset:0x800
	ds_read_b128 v[188:191], v210 offset:0x1000
	ds_read_b128 v[192:195], v210 offset:0x1800
	ds_read_b128 v[212:215], v209 offset:0
	ds_read_b128 v[216:219], v209 offset:0x800
	ds_read_b128 v[220:223], v209 offset:0x1000
	s_waitcnt lgkmcnt(0)
	s_add_u32 s0, s10, s0
	s_addc_u32 s18, s11, s1
	s_lshl_b32 s19, s24, 1
	s_mov_b32 s1, 0
	s_add_u32 s0, s0, s19
	s_waitcnt lgkmcnt(2)
	s_addc_u32 s20, s18, 0
	v_mfma_f32_16x16x32_bf16 v[174:177], v[180:183], v[212:215], v[174:177]
	v_mfma_f32_16x16x32_bf16 v[170:173], v[184:187], v[212:215], v[170:173]
	v_mfma_f32_16x16x32_bf16 v[166:169], v[188:191], v[212:215], v[166:169]
	v_mfma_f32_16x16x32_bf16 v[162:165], v[192:195], v[212:215], v[162:165]
	ds_read_b128 v[212:215], v209 offset:0x1800
	s_waitcnt lgkmcnt(2)
	v_mfma_f32_16x16x32_bf16 v[158:161], v[180:183], v[216:219], v[158:161]
	v_mfma_f32_16x16x32_bf16 v[154:157], v[184:187], v[216:219], v[154:157]
	v_mfma_f32_16x16x32_bf16 v[150:153], v[188:191], v[216:219], v[150:153]
	v_mfma_f32_16x16x32_bf16 v[146:149], v[192:195], v[216:219], v[146:149]
	ds_read_b128 v[216:219], v209 offset:0x2000
	s_waitcnt lgkmcnt(2)
	v_mfma_f32_16x16x32_bf16 v[142:145], v[180:183], v[220:223], v[142:145]
	v_mfma_f32_16x16x32_bf16 v[138:141], v[184:187], v[220:223], v[138:141]
	v_mfma_f32_16x16x32_bf16 v[134:137], v[188:191], v[220:223], v[134:137]
	v_mfma_f32_16x16x32_bf16 v[130:133], v[192:195], v[220:223], v[130:133]
	ds_read_b128 v[220:223], v209 offset:0x2800
	s_waitcnt lgkmcnt(2)
	v_mfma_f32_16x16x32_bf16 v[126:129], v[180:183], v[212:215], v[126:129]
	v_mfma_f32_16x16x32_bf16 v[122:125], v[184:187], v[212:215], v[122:125]
	v_mfma_f32_16x16x32_bf16 v[118:121], v[188:191], v[212:215], v[118:121]
	v_mfma_f32_16x16x32_bf16 v[114:117], v[192:195], v[212:215], v[114:117]
	ds_read_b128 v[212:215], v209 offset:0x3000
	s_waitcnt lgkmcnt(2)
	v_mfma_f32_16x16x32_bf16 v[110:113], v[180:183], v[216:219], v[110:113]
	v_mfma_f32_16x16x32_bf16 v[106:109], v[184:187], v[216:219], v[106:109]
	v_mfma_f32_16x16x32_bf16 v[102:105], v[188:191], v[216:219], v[102:105]
	v_mfma_f32_16x16x32_bf16 v[98:101], v[192:195], v[216:219], v[98:101]
	ds_read_b128 v[216:219], v209 offset:0x3800
	s_waitcnt lgkmcnt(2)
	v_mfma_f32_16x16x32_bf16 v[94:97], v[180:183], v[220:223], v[94:97]
	v_mfma_f32_16x16x32_bf16 v[90:93], v[184:187], v[220:223], v[90:93]
	v_mfma_f32_16x16x32_bf16 v[86:89], v[188:191], v[220:223], v[86:89]
	v_mfma_f32_16x16x32_bf16 v[82:85], v[192:195], v[220:223], v[82:85]
	s_waitcnt lgkmcnt(1)
	v_mfma_f32_16x16x32_bf16 v[78:81], v[180:183], v[212:215], v[78:81]
	v_mfma_f32_16x16x32_bf16 v[74:77], v[184:187], v[212:215], v[74:77]
	v_mfma_f32_16x16x32_bf16 v[70:73], v[188:191], v[212:215], v[70:73]
	v_mfma_f32_16x16x32_bf16 v[66:69], v[192:195], v[212:215], v[66:69]
	s_waitcnt lgkmcnt(0)
	v_mfma_f32_16x16x32_bf16 v[62:65], v[180:183], v[216:219], v[62:65]
	v_mfma_f32_16x16x32_bf16 v[58:61], v[184:187], v[216:219], v[58:61]
	v_mfma_f32_16x16x32_bf16 v[54:57], v[188:191], v[216:219], v[54:57]
	v_mfma_f32_16x16x32_bf16 v[50:53], v[192:195], v[216:219], v[50:53]
	s_add_i32 s18, 0, 0x10000
	s_waitcnt vmcnt(10)
	v_cvt_pk_bf16_f32 v46, v46, v47
	v_cvt_pk_bf16_f32 v47, v48, v49
	v_cvt_pk_bf16_f32 v48, v42, v43
	v_add_u32_e32 v42, s18, v208
	s_waitcnt vmcnt(8)
	v_cvt_pk_bf16_f32 v38, v38, v39
	v_cvt_pk_bf16_f32 v39, v40, v41
	v_cvt_pk_bf16_f32 v40, v34, v35
	v_add_u32_e32 v34, s18, v205
	s_add_i32 s19, 0, 0x18000
	v_cvt_pk_bf16_f32 v49, v44, v45
	ds_write_b128 v42, v[46:49]
	v_cvt_pk_bf16_f32 v41, v36, v37
	ds_write_b128 v34, v[38:41]
	v_add_u32_e32 v34, s19, v206
	s_waitcnt vmcnt(7)
	ds_write_b128 v34, v[30:33]
	v_add_u32_e32 v30, s19, v207
	s_waitcnt vmcnt(6)
	ds_write_b128 v30, v[26:29]
	ds_read_b128 v[26:29], v210 offset:0x400
	ds_read_b128 v[30:33], v210 offset:0xc00
	ds_read_b128 v[34:37], v210 offset:0x1400
	ds_read_b128 v[38:41], v210 offset:0x1c00
	ds_read_b128 v[42:45], v209 offset:0x400
	ds_read_b128 v[46:49], v209 offset:0xc00
	ds_read_b128 v[180:183], v209 offset:0x1400
	s_waitcnt lgkmcnt(2)
	v_mfma_f32_16x16x32_bf16 v[174:177], v[26:29], v[42:45], v[174:177]
	v_mfma_f32_16x16x32_bf16 v[170:173], v[30:33], v[42:45], v[170:173]
	v_mfma_f32_16x16x32_bf16 v[166:169], v[34:37], v[42:45], v[166:169]
	v_mfma_f32_16x16x32_bf16 v[42:45], v[38:41], v[42:45], v[162:165]
	ds_read_b128 v[162:165], v209 offset:0x1c00
	s_waitcnt lgkmcnt(2)
	v_mfma_f32_16x16x32_bf16 v[158:161], v[26:29], v[46:49], v[158:161]
	v_mfma_f32_16x16x32_bf16 v[154:157], v[30:33], v[46:49], v[154:157]
	v_mfma_f32_16x16x32_bf16 v[150:153], v[34:37], v[46:49], v[150:153]
	v_mfma_f32_16x16x32_bf16 v[46:49], v[38:41], v[46:49], v[146:149]
	ds_read_b128 v[146:149], v209 offset:0x2400
	s_waitcnt lgkmcnt(2)
	v_mfma_f32_16x16x32_bf16 v[142:145], v[26:29], v[180:183], v[142:145]
	v_mfma_f32_16x16x32_bf16 v[138:141], v[30:33], v[180:183], v[138:141]
	v_mfma_f32_16x16x32_bf16 v[134:137], v[34:37], v[180:183], v[134:137]
	v_mfma_f32_16x16x32_bf16 v[130:133], v[38:41], v[180:183], v[130:133]
	ds_read_b128 v[180:183], v209 offset:0x2c00
	s_waitcnt lgkmcnt(2)
	v_mfma_f32_16x16x32_bf16 v[126:129], v[26:29], v[162:165], v[126:129]
	v_mfma_f32_16x16x32_bf16 v[122:125], v[30:33], v[162:165], v[122:125]
	v_mfma_f32_16x16x32_bf16 v[118:121], v[34:37], v[162:165], v[118:121]
	v_mfma_f32_16x16x32_bf16 v[114:117], v[38:41], v[162:165], v[114:117]
	ds_read_b128 v[162:165], v209 offset:0x3400
	s_waitcnt lgkmcnt(2)
	v_mfma_f32_16x16x32_bf16 v[110:113], v[26:29], v[146:149], v[110:113]
	v_mfma_f32_16x16x32_bf16 v[106:109], v[30:33], v[146:149], v[106:109]
	v_mfma_f32_16x16x32_bf16 v[102:105], v[34:37], v[146:149], v[102:105]
	v_mfma_f32_16x16x32_bf16 v[98:101], v[38:41], v[146:149], v[98:101]
	ds_read_b128 v[146:149], v209 offset:0x3c00
	s_waitcnt lgkmcnt(2)
	v_mfma_f32_16x16x32_bf16 v[94:97], v[26:29], v[180:183], v[94:97]
	v_mfma_f32_16x16x32_bf16 v[90:93], v[30:33], v[180:183], v[90:93]
	v_mfma_f32_16x16x32_bf16 v[86:89], v[34:37], v[180:183], v[86:89]
	v_mfma_f32_16x16x32_bf16 v[82:85], v[38:41], v[180:183], v[82:85]
	s_waitcnt lgkmcnt(1)
	v_mfma_f32_16x16x32_bf16 v[78:81], v[26:29], v[162:165], v[78:81]
	v_mfma_f32_16x16x32_bf16 v[74:77], v[30:33], v[162:165], v[74:77]
	v_mfma_f32_16x16x32_bf16 v[70:73], v[34:37], v[162:165], v[70:73]
	v_mfma_f32_16x16x32_bf16 v[66:69], v[38:41], v[162:165], v[66:69]
	s_waitcnt lgkmcnt(0)
	v_mfma_f32_16x16x32_bf16 v[26:29], v[26:29], v[146:149], v[62:65]
	v_mfma_f32_16x16x32_bf16 v[30:33], v[30:33], v[146:149], v[58:61]
	v_mfma_f32_16x16x32_bf16 v[34:37], v[34:37], v[146:149], v[54:57]
	v_mfma_f32_16x16x32_bf16 v[38:41], v[38:41], v[146:149], v[50:53]
	s_waitcnt vmcnt(4)
	v_cvt_pk_bf16_f32 v22, v22, v23
	v_cvt_pk_bf16_f32 v23, v24, v25
	v_cvt_pk_bf16_f32 v24, v6, v7
	v_cvt_pk_bf16_f32 v25, v8, v9
	v_add_u32_e32 v6, s18, v204
	s_waitcnt vmcnt(3)
	v_cvt_pk_bf16_f32 v8, v2, v3
	v_add_u32_e32 v2, s18, v201
	ds_write_b128 v6, v[22:25]
	s_waitcnt vmcnt(2)
	v_cvt_pk_bf16_f32 v6, v10, v11
	v_cvt_pk_bf16_f32 v7, v12, v13
	v_cvt_pk_bf16_f32 v9, v4, v5
	ds_write_b128 v2, v[6:9]
	v_add_u32_e32 v2, s19, v202
	s_waitcnt vmcnt(1)
	ds_write_b128 v2, v[18:21]
	v_add_u32_e32 v2, s19, v203
	s_waitcnt vmcnt(0)
	ds_write_b128 v2, v[14:17]
	s_waitcnt lgkmcnt(0)
	s_barrier
	v_add_u32_e32 v178, 0x10000, v209
	v_add_u32_e32 v196, 0x10000, v210
	ds_read_b128 v[2:5], v196 offset:0
	ds_read_b128 v[6:9], v196 offset:0x800
	ds_read_b128 v[10:13], v196 offset:0x1000
	ds_read_b128 v[14:17], v196 offset:0x1800
	ds_read_b128 v[18:21], v178 offset:0
	s_and_b64 s[16:17], s[16:17], exec
	ds_read_b128 v[22:25], v178 offset:0x800
	ds_read_b128 v[50:53], v178 offset:0x1000
	s_waitcnt lgkmcnt(2)
	s_cselect_b32 s5, s5, s7
	s_cselect_b32 s4, s4, s6
	s_lshl_b32 s6, s3, 10
	v_mfma_f32_16x16x32_bf16 v[54:57], v[2:5], v[18:21], v[174:177]
	s_add_u32 s6, s4, s6
	s_addc_u32 s7, s5, 0
	s_lshl_b32 s3, s3, 9
	v_mfma_f32_16x16x32_bf16 v[58:61], v[6:9], v[18:21], v[170:173]
	s_add_u32 s4, s0, s3
	s_addc_u32 s5, s20, 0
	v_mfma_f32_16x16x32_bf16 v[62:65], v[10:13], v[18:21], v[166:169]
	v_mfma_f32_16x16x32_bf16 v[18:21], v[14:17], v[18:21], v[42:45]
	ds_read_b128 v[42:45], v178 offset:0x1800
	s_waitcnt lgkmcnt(2)
	v_mfma_f32_16x16x32_bf16 v[146:149], v[2:5], v[22:25], v[158:161]
	v_mfma_f32_16x16x32_bf16 v[154:157], v[6:9], v[22:25], v[154:157]
	v_mfma_f32_16x16x32_bf16 v[150:153], v[10:13], v[22:25], v[150:153]
	v_mfma_f32_16x16x32_bf16 v[22:25], v[14:17], v[22:25], v[46:49]
	ds_read_b128 v[46:49], v178 offset:0x2000
	s_waitcnt lgkmcnt(2)
	v_mfma_f32_16x16x32_bf16 v[142:145], v[2:5], v[50:53], v[142:145]
	v_mfma_f32_16x16x32_bf16 v[138:141], v[6:9], v[50:53], v[138:141]
	v_mfma_f32_16x16x32_bf16 v[134:137], v[10:13], v[50:53], v[134:137]
	v_mfma_f32_16x16x32_bf16 v[50:53], v[14:17], v[50:53], v[130:133]
	ds_read_b128 v[130:133], v178 offset:0x2800
	s_waitcnt lgkmcnt(2)
	v_mfma_f32_16x16x32_bf16 v[126:129], v[2:5], v[42:45], v[126:129]
	v_mfma_f32_16x16x32_bf16 v[122:125], v[6:9], v[42:45], v[122:125]
	v_mfma_f32_16x16x32_bf16 v[118:121], v[10:13], v[42:45], v[118:121]
	v_mfma_f32_16x16x32_bf16 v[42:45], v[14:17], v[42:45], v[114:117]
	ds_read_b128 v[114:117], v178 offset:0x3000
	s_waitcnt lgkmcnt(2)
	v_mfma_f32_16x16x32_bf16 v[110:113], v[2:5], v[46:49], v[110:113]
	v_mfma_f32_16x16x32_bf16 v[106:109], v[6:9], v[46:49], v[106:109]
	v_mfma_f32_16x16x32_bf16 v[102:105], v[10:13], v[46:49], v[102:105]
	v_mfma_f32_16x16x32_bf16 v[98:101], v[14:17], v[46:49], v[98:101]
	ds_read_b128 v[46:49], v178 offset:0x3800
	s_waitcnt lgkmcnt(2)
	v_mfma_f32_16x16x32_bf16 v[158:161], v[2:5], v[130:133], v[94:97]
	v_mfma_f32_16x16x32_bf16 v[162:165], v[6:9], v[130:133], v[90:93]
	v_mfma_f32_16x16x32_bf16 v[166:169], v[10:13], v[130:133], v[86:89]
	v_mfma_f32_16x16x32_bf16 v[130:133], v[14:17], v[130:133], v[82:85]
	s_waitcnt lgkmcnt(1)
	v_mfma_f32_16x16x32_bf16 v[66:69], v[14:17], v[114:117], v[66:69]
	v_mfma_f32_16x16x32_bf16 v[170:173], v[2:5], v[114:117], v[78:81]
	v_mfma_f32_16x16x32_bf16 v[174:177], v[6:9], v[114:117], v[74:77]
	v_mfma_f32_16x16x32_bf16 v[180:183], v[10:13], v[114:117], v[70:73]
	s_waitcnt lgkmcnt(0)
	v_mfma_f32_16x16x32_bf16 v[2:5], v[2:5], v[46:49], v[26:29]
	v_mfma_f32_16x16x32_bf16 v[114:117], v[6:9], v[46:49], v[30:33]
	v_mfma_f32_16x16x32_bf16 v[34:37], v[10:13], v[46:49], v[34:37]
	v_mfma_f32_16x16x32_bf16 v[184:187], v[14:17], v[46:49], v[38:41]
	ds_read_b128 v[188:191], v196 offset:0x400
	ds_read_b128 v[192:195], v196 offset:0xc00
	ds_read_b128 v[202:205], v196 offset:0x1400
	ds_read_b128 v[206:209], v196 offset:0x1c00
	ds_read_b128 v[6:9], v178 offset:0x400
	ds_read_b128 v[10:13], v178 offset:0xc00
	ds_read_b128 v[14:17], v178 offset:0x1400
	s_waitcnt lgkmcnt(2)
	v_mfma_f32_16x16x32_bf16 v[94:97], v[192:195], v[6:9], v[58:61]
	v_mfma_f32_16x16x32_bf16 v[62:65], v[202:205], v[6:9], v[62:65]
	v_mfma_f32_16x16x32_bf16 v[30:33], v[206:209], v[6:9], v[18:21]
	v_mfma_f32_16x16x32_bf16 v[210:213], v[188:191], v[6:9], v[54:57]
	ds_read_b128 v[6:9], v178 offset:0x1c00
	s_waitcnt lgkmcnt(2)
	v_mfma_f32_16x16x32_bf16 v[90:93], v[192:195], v[10:13], v[154:157]
	v_mfma_f32_16x16x32_bf16 v[58:61], v[202:205], v[10:13], v[150:153]
	v_mfma_f32_16x16x32_bf16 v[26:29], v[206:209], v[10:13], v[22:25]
	v_mfma_f32_16x16x32_bf16 v[146:149], v[188:191], v[10:13], v[146:149]
	ds_read_b128 v[10:13], v178 offset:0x2400
	s_waitcnt lgkmcnt(2)
	v_mfma_f32_16x16x32_bf16 v[86:89], v[192:195], v[14:17], v[138:141]
	v_mfma_f32_16x16x32_bf16 v[54:57], v[202:205], v[14:17], v[134:137]
	v_mfma_f32_16x16x32_bf16 v[22:25], v[206:209], v[14:17], v[50:53]
	v_mfma_f32_16x16x32_bf16 v[142:145], v[188:191], v[14:17], v[142:145]
	ds_read_b128 v[38:41], v178 offset:0x2c00
	s_waitcnt lgkmcnt(2)
	v_mfma_f32_16x16x32_bf16 v[126:129], v[188:191], v[6:9], v[126:129]
	v_mfma_f32_16x16x32_bf16 v[82:85], v[192:195], v[6:9], v[122:125]
	v_mfma_f32_16x16x32_bf16 v[50:53], v[202:205], v[6:9], v[118:121]
	v_mfma_f32_16x16x32_bf16 v[18:21], v[206:209], v[6:9], v[42:45]
	ds_read_b128 v[6:9], v178 offset:0x3400
	s_waitcnt lgkmcnt(2)
	v_mfma_f32_16x16x32_bf16 v[110:113], v[188:191], v[10:13], v[110:113]
	v_mfma_f32_16x16x32_bf16 v[78:81], v[192:195], v[10:13], v[106:109]
	v_mfma_f32_16x16x32_bf16 v[46:49], v[202:205], v[10:13], v[102:105]
	v_mfma_f32_16x16x32_bf16 v[14:17], v[206:209], v[10:13], v[98:101]
	ds_read_b128 v[98:101], v178 offset:0x3c00
	s_waitcnt lgkmcnt(2)
	v_mfma_f32_16x16x32_bf16 v[106:109], v[188:191], v[38:41], v[158:161]
	v_mfma_f32_16x16x32_bf16 v[74:77], v[192:195], v[38:41], v[162:165]
	v_mfma_f32_16x16x32_bf16 v[42:45], v[202:205], v[38:41], v[166:169]
	v_mfma_f32_16x16x32_bf16 v[10:13], v[206:209], v[38:41], v[130:133]
	s_waitcnt lgkmcnt(1)
	v_mfma_f32_16x16x32_bf16 v[118:121], v[188:191], v[6:9], v[170:173]
	v_mfma_f32_16x16x32_bf16 v[70:73], v[192:195], v[6:9], v[174:177]
	v_mfma_f32_16x16x32_bf16 v[38:41], v[202:205], v[6:9], v[180:183]
	v_mfma_f32_16x16x32_bf16 v[6:9], v[206:209], v[6:9], v[66:69]
	s_waitcnt lgkmcnt(0)
	v_mfma_f32_16x16x32_bf16 v[122:125], v[188:191], v[98:101], v[2:5]
	v_mfma_f32_16x16x32_bf16 v[66:69], v[192:195], v[98:101], v[114:117]
	v_mfma_f32_16x16x32_bf16 v[34:37], v[202:205], v[98:101], v[34:37]
	v_mfma_f32_16x16x32_bf16 v[2:5], v[206:209], v[98:101], v[184:187]
	v_lshrrev_b32_e32 v98, 2, v199
	v_and_b32_e32 v98, 12, v98
	v_lshl_or_b32 v104, v200, 6, v98
	v_lshlrev_b32_e32 v105, 2, v104
	s_waitcnt lgkmcnt(0)
	s_barrier
	global_load_dwordx4 v[114:117], v105, s[6:7]
	v_lshrrev_b32_e32 v98, 1, v199
	v_lshlrev_b32_e32 v99, 16, v198
	v_lshlrev_b32_e32 v100, 9, v179
	v_and_b32_e32 v102, 8, v98
	v_lshrrev_b32_e32 v98, 3, v104
	v_add3_u32 v103, 0, v99, v100
	v_xor_b32_e32 v130, v98, v179
	v_bitop3_b32 v131, v98, v179, 16 bitop3:0x1e
	global_load_dwordx4 v[98:101], v105, s[6:7] offset:64
	v_lshlrev_b32_e32 v130, 4, v130
	v_lshlrev_b32_e32 v131, 4, v131
	v_add3_u32 v130, v103, v130, v102
	v_add3_u32 v131, v103, v131, v102
	s_movk_i32 s0, 0x200
	s_waitcnt vmcnt(1)
	v_add_f32_e32 v132, v210, v114
	v_add_f32_e32 v133, v211, v115
	v_add_f32_e32 v134, v212, v116
	v_add_f32_e32 v135, v213, v117
	v_add_f32_e32 v140, v142, v114
	v_add_f32_e32 v141, v143, v115
	v_add_f32_e32 v142, v144, v116
	v_add_f32_e32 v143, v145, v117
	v_add_f32_e32 v110, v110, v114
	v_add_f32_e32 v111, v111, v115
	v_add_f32_e32 v106, v106, v114
	v_add_f32_e32 v107, v107, v115
	v_add_f32_e32 v136, v146, v114
	v_add_f32_e32 v137, v147, v115
	v_add_f32_e32 v138, v148, v116
	v_add_f32_e32 v139, v149, v117
	v_add_f32_e32 v126, v126, v114
	v_add_f32_e32 v127, v127, v115
	v_add_f32_e32 v128, v128, v116
	v_add_f32_e32 v129, v129, v117
	v_add_f32_e32 v112, v112, v116
	v_add_f32_e32 v113, v113, v117
	v_add_f32_e32 v108, v108, v116
	v_add_f32_e32 v109, v109, v117
	v_max_f32_e32 v132, 0, v132
	v_max_f32_e32 v133, 0, v133
	v_max_f32_e32 v134, 0, v134
	v_max_f32_e32 v135, 0, v135
	v_max_f32_e32 v140, 0, v140
	v_max_f32_e32 v141, 0, v141
	v_max_f32_e32 v142, 0, v142
	v_max_f32_e32 v143, 0, v143
	v_max_f32_e32 v144, 0, v110
	v_max_f32_e32 v145, 0, v111
	v_max_f32_e32 v148, 0, v106
	v_max_f32_e32 v149, 0, v107
	v_cvt_pk_bf16_f32 v106, v132, v133
	v_cvt_pk_bf16_f32 v107, v134, v135
	v_cvt_pk_bf16_f32 v110, v140, v141
	v_cvt_pk_bf16_f32 v111, v142, v143
	v_add_f32_e32 v118, v118, v114
	v_add_f32_e32 v119, v119, v115
	v_max_f32_e32 v136, 0, v136
	v_max_f32_e32 v137, 0, v137
	v_max_f32_e32 v138, 0, v138
	v_max_f32_e32 v139, 0, v139
	v_max_f32_e32 v126, 0, v126
	v_max_f32_e32 v127, 0, v127
	v_max_f32_e32 v128, 0, v128
	v_max_f32_e32 v129, 0, v129
	v_max_f32_e32 v146, 0, v112
	v_max_f32_e32 v147, 0, v113
	v_max_f32_e32 v150, 0, v108
	v_max_f32_e32 v151, 0, v109
	v_cvt_pk_bf16_f32 v108, v136, v137
	v_cvt_pk_bf16_f32 v109, v138, v139
	v_cvt_pk_bf16_f32 v112, v126, v127
	v_cvt_pk_bf16_f32 v113, v128, v129
	ds_write2st64_b64 v130, v[106:107], v[110:111] offset1:32
	ds_write2st64_b64 v131, v[108:109], v[112:113] offset0:16 offset1:48
	v_add_f32_e32 v106, v121, v117
	v_add_f32_e32 v120, v120, v116
	v_max_f32_e32 v152, 0, v118
	v_max_f32_e32 v153, 0, v119
	v_max_f32_e32 v107, 0, v106
	v_cvt_pk_bf16_f32 v106, v152, v153
	v_max_f32_e32 v120, 0, v120
	v_cvt_pk_bf16_f32 v118, v144, v145
	v_cvt_pk_bf16_f32 v119, v146, v147
	v_cvt_pk_bf16_f32 v107, v120, v107
	ds_write2st64_b64 v130, v[118:119], v[106:107] offset0:64 offset1:96
	v_add_f32_e32 v106, v122, v114
	v_max_f32_e32 v106, 0, v106
	v_add_f32_e32 v107, v123, v115
	v_max_f32_e32 v107, 0, v107
	v_add_f32_e32 v108, v124, v116
	v_add_f32_e32 v109, v125, v117
	v_cvt_pk_bf16_f32 v106, v106, v107
	v_cvt_pk_bf16_f32 v126, v148, v149
	v_cvt_pk_bf16_f32 v127, v150, v151
	v_max_f32_e32 v108, 0, v108
	v_max_f32_e32 v109, 0, v109
	v_cvt_pk_bf16_f32 v107, v108, v109
	ds_write2st64_b64 v131, v[126:127], v[106:107] offset0:80 offset1:112
	v_or_b32_e32 v106, 16, v104
	s_waitcnt vmcnt(0)
	v_add_f32_e32 v94, v94, v98
	v_add_f32_e32 v95, v95, v99
	v_add_f32_e32 v96, v96, v100
	v_lshrrev_b32_e32 v106, 3, v106
	v_max_f32_e32 v94, 0, v94
	v_max_f32_e32 v95, 0, v95
	v_max_f32_e32 v96, 0, v96
	v_add_f32_e32 v97, v97, v101
	v_max_f32_e32 v97, 0, v97
	v_cvt_pk_bf16_f32 v94, v94, v95
	v_cvt_pk_bf16_f32 v95, v96, v97
	v_xor_b32_e32 v96, v106, v179
	v_lshlrev_b32_e32 v96, 4, v96
	v_add3_u32 v107, v103, v96, v102
	v_add_f32_e32 v90, v90, v98
	v_add_f32_e32 v91, v91, v99
	v_add_f32_e32 v92, v92, v100
	ds_write_b64 v107, v[94:95]
	v_max_f32_e32 v90, 0, v90
	v_max_f32_e32 v91, 0, v91
	global_load_dwordx4 v[94:97], v105, s[6:7] offset:128
	v_max_f32_e32 v92, 0, v92
	v_add_f32_e32 v93, v93, v101
	v_max_f32_e32 v93, 0, v93
	v_cvt_pk_bf16_f32 v90, v90, v91
	v_cvt_pk_bf16_f32 v91, v92, v93
	v_bitop3_b32 v92, v106, v179, 16 bitop3:0x1e
	v_add_f32_e32 v66, v66, v98
	v_lshlrev_b32_e32 v92, 4, v92
	v_add_f32_e32 v86, v86, v98
	v_add_f32_e32 v87, v87, v99
	v_add_f32_e32 v82, v82, v98
	v_add_f32_e32 v83, v83, v99
	v_add_f32_e32 v78, v78, v98
	v_add_f32_e32 v79, v79, v99
	v_add_f32_e32 v74, v74, v98
	v_add_f32_e32 v75, v75, v99
	v_add_f32_e32 v70, v70, v98
	v_add_f32_e32 v71, v71, v99
	v_max_f32_e32 v66, 0, v66
	v_add_f32_e32 v67, v67, v99
	v_add3_u32 v92, v103, v92, v102
	v_max_f32_e32 v86, 0, v86
	v_max_f32_e32 v87, 0, v87
	v_add_f32_e32 v88, v88, v100
	v_add_f32_e32 v89, v89, v101
	v_max_f32_e32 v82, 0, v82
	v_max_f32_e32 v83, 0, v83
	v_add_f32_e32 v84, v84, v100
	v_add_f32_e32 v85, v85, v101
	v_max_f32_e32 v78, 0, v78
	v_max_f32_e32 v79, 0, v79
	v_add_f32_e32 v80, v80, v100
	v_add_f32_e32 v81, v81, v101
	v_max_f32_e32 v74, 0, v74
	v_max_f32_e32 v75, 0, v75
	v_add_f32_e32 v76, v76, v100
	v_add_f32_e32 v77, v77, v101
	v_max_f32_e32 v70, 0, v70
	v_max_f32_e32 v71, 0, v71
	v_add_f32_e32 v72, v72, v100
	v_add_f32_e32 v73, v73, v101
	v_max_f32_e32 v67, 0, v67
	v_add_f32_e32 v68, v68, v100
	v_add_f32_e32 v69, v69, v101
	v_cvt_pk_bf16_f32 v66, v66, v67
	ds_write_b64 v92, v[90:91] offset:8192
	v_max_f32_e32 v88, 0, v88
	v_max_f32_e32 v89, 0, v89
	v_cvt_pk_bf16_f32 v86, v86, v87
	v_cvt_pk_bf16_f32 v87, v88, v89
	ds_write_b64 v107, v[86:87] offset:16384
	v_max_f32_e32 v84, 0, v84
	v_max_f32_e32 v85, 0, v85
	v_cvt_pk_bf16_f32 v82, v82, v83
	v_cvt_pk_bf16_f32 v83, v84, v85
	ds_write_b64 v92, v[82:83] offset:24576
	v_max_f32_e32 v80, 0, v80
	v_max_f32_e32 v81, 0, v81
	v_cvt_pk_bf16_f32 v78, v78, v79
	v_cvt_pk_bf16_f32 v79, v80, v81
	ds_write_b64 v107, v[78:79] offset:32768
	v_max_f32_e32 v76, 0, v76
	v_max_f32_e32 v77, 0, v77
	v_cvt_pk_bf16_f32 v74, v74, v75
	v_cvt_pk_bf16_f32 v75, v76, v77
	ds_write_b64 v92, v[74:75] offset:40960
	v_max_f32_e32 v72, 0, v72
	v_max_f32_e32 v73, 0, v73
	v_cvt_pk_bf16_f32 v70, v70, v71
	v_cvt_pk_bf16_f32 v71, v72, v73
	ds_write_b64 v107, v[70:71] offset:49152
	v_max_f32_e32 v68, 0, v68
	v_max_f32_e32 v69, 0, v69
	v_cvt_pk_bf16_f32 v67, v68, v69
	ds_write_b64 v92, v[66:67] offset:57344
	v_or_b32_e32 v66, 32, v104
	v_lshrrev_b32_e32 v70, 3, v66
	global_load_dwordx4 v[66:69], v105, s[6:7] offset:192
	s_waitcnt vmcnt(1)
	v_add_f32_e32 v62, v62, v94
	v_add_f32_e32 v63, v63, v95
	v_add_f32_e32 v64, v64, v96
	v_add_f32_e32 v58, v58, v94
	v_add_f32_e32 v59, v59, v95
	v_add_f32_e32 v60, v60, v96
	v_max_f32_e32 v62, 0, v62
	v_max_f32_e32 v63, 0, v63
	v_max_f32_e32 v64, 0, v64
	v_add_f32_e32 v65, v65, v97
	v_max_f32_e32 v58, 0, v58
	v_max_f32_e32 v59, 0, v59
	v_max_f32_e32 v60, 0, v60
	v_add_f32_e32 v61, v61, v97
	v_max_f32_e32 v65, 0, v65
	v_cvt_pk_bf16_f32 v62, v62, v63
	v_cvt_pk_bf16_f32 v63, v64, v65
	v_xor_b32_e32 v64, v70, v179
	v_max_f32_e32 v61, 0, v61
	v_cvt_pk_bf16_f32 v58, v58, v59
	v_cvt_pk_bf16_f32 v59, v60, v61
	v_bitop3_b32 v60, v70, v179, 16 bitop3:0x1e
	v_add_f32_e32 v34, v34, v94
	v_lshlrev_b32_e32 v64, 4, v64
	v_lshlrev_b32_e32 v60, 4, v60
	v_add_f32_e32 v54, v54, v94
	v_add_f32_e32 v55, v55, v95
	v_add_f32_e32 v50, v50, v94
	v_add_f32_e32 v51, v51, v95
	v_add_f32_e32 v46, v46, v94
	v_add_f32_e32 v47, v47, v95
	v_add_f32_e32 v42, v42, v94
	v_add_f32_e32 v43, v43, v95
	v_add_f32_e32 v38, v38, v94
	v_add_f32_e32 v39, v39, v95
	v_max_f32_e32 v34, 0, v34
	v_add_f32_e32 v35, v35, v95
	v_add3_u32 v64, v103, v64, v102
	v_add3_u32 v60, v103, v60, v102
	v_max_f32_e32 v54, 0, v54
	v_max_f32_e32 v55, 0, v55
	v_add_f32_e32 v56, v56, v96
	v_add_f32_e32 v57, v57, v97
	v_max_f32_e32 v50, 0, v50
	v_max_f32_e32 v51, 0, v51
	v_add_f32_e32 v52, v52, v96
	v_add_f32_e32 v53, v53, v97
	v_max_f32_e32 v46, 0, v46
	v_max_f32_e32 v47, 0, v47
	v_add_f32_e32 v48, v48, v96
	v_add_f32_e32 v49, v49, v97
	v_max_f32_e32 v42, 0, v42
	v_max_f32_e32 v43, 0, v43
	v_add_f32_e32 v44, v44, v96
	v_add_f32_e32 v45, v45, v97
	v_max_f32_e32 v38, 0, v38
	v_max_f32_e32 v39, 0, v39
	v_add_f32_e32 v40, v40, v96
	v_add_f32_e32 v41, v41, v97
	v_max_f32_e32 v35, 0, v35
	v_add_f32_e32 v36, v36, v96
	v_add_f32_e32 v37, v37, v97
	v_cvt_pk_bf16_f32 v34, v34, v35
	ds_write_b64 v64, v[62:63]
	ds_write_b64 v60, v[58:59] offset:8192
	v_max_f32_e32 v56, 0, v56
	v_max_f32_e32 v57, 0, v57
	v_cvt_pk_bf16_f32 v54, v54, v55
	v_cvt_pk_bf16_f32 v55, v56, v57
	ds_write_b64 v64, v[54:55] offset:16384
	v_max_f32_e32 v52, 0, v52
	v_max_f32_e32 v53, 0, v53
	v_cvt_pk_bf16_f32 v50, v50, v51
	v_cvt_pk_bf16_f32 v51, v52, v53
	ds_write_b64 v60, v[50:51] offset:24576
	v_max_f32_e32 v48, 0, v48
	v_max_f32_e32 v49, 0, v49
	v_cvt_pk_bf16_f32 v46, v46, v47
	v_cvt_pk_bf16_f32 v47, v48, v49
	ds_write_b64 v64, v[46:47] offset:32768
	v_max_f32_e32 v44, 0, v44
	v_max_f32_e32 v45, 0, v45
	v_cvt_pk_bf16_f32 v42, v42, v43
	v_cvt_pk_bf16_f32 v43, v44, v45
	ds_write_b64 v60, v[42:43] offset:40960
	v_max_f32_e32 v40, 0, v40
	v_max_f32_e32 v41, 0, v41
	v_cvt_pk_bf16_f32 v38, v38, v39
	v_cvt_pk_bf16_f32 v39, v40, v41
	ds_write_b64 v64, v[38:39] offset:49152
	v_max_f32_e32 v36, 0, v36
	v_max_f32_e32 v37, 0, v37
	v_cvt_pk_bf16_f32 v35, v36, v37
	ds_write_b64 v60, v[34:35] offset:57344
	v_or_b32_e32 v34, 48, v104
	s_waitcnt vmcnt(0)
	v_add_f32_e32 v30, v30, v66
	v_add_f32_e32 v31, v31, v67
	v_add_f32_e32 v32, v32, v68
	v_add_f32_e32 v26, v26, v66
	v_add_f32_e32 v27, v27, v67
	v_add_f32_e32 v28, v28, v68
	v_lshrrev_b32_e32 v34, 3, v34
	v_max_f32_e32 v30, 0, v30
	v_max_f32_e32 v31, 0, v31
	v_max_f32_e32 v32, 0, v32
	v_add_f32_e32 v33, v33, v69
	v_max_f32_e32 v26, 0, v26
	v_max_f32_e32 v27, 0, v27
	v_max_f32_e32 v28, 0, v28
	v_add_f32_e32 v29, v29, v69
	v_max_f32_e32 v33, 0, v33
	v_cvt_pk_bf16_f32 v30, v30, v31
	v_cvt_pk_bf16_f32 v31, v32, v33
	v_xor_b32_e32 v32, v34, v179
	v_max_f32_e32 v29, 0, v29
	v_cvt_pk_bf16_f32 v26, v26, v27
	v_cvt_pk_bf16_f32 v27, v28, v29
	v_bitop3_b32 v28, v34, v179, 16 bitop3:0x1e
	v_add_f32_e32 v2, v2, v66
	v_lshlrev_b32_e32 v32, 4, v32
	v_lshlrev_b32_e32 v28, 4, v28
	v_add_f32_e32 v22, v22, v66
	v_add_f32_e32 v23, v23, v67
	v_add_f32_e32 v18, v18, v66
	v_add_f32_e32 v19, v19, v67
	v_add_f32_e32 v14, v14, v66
	v_add_f32_e32 v15, v15, v67
	v_add_f32_e32 v10, v10, v66
	v_add_f32_e32 v11, v11, v67
	v_add_f32_e32 v6, v6, v66
	v_add_f32_e32 v7, v7, v67
	v_max_f32_e32 v2, 0, v2
	v_add_f32_e32 v3, v3, v67
	v_add3_u32 v32, v103, v32, v102
	v_add3_u32 v28, v103, v28, v102
	v_max_f32_e32 v22, 0, v22
	v_max_f32_e32 v23, 0, v23
	v_add_f32_e32 v24, v24, v68
	v_add_f32_e32 v25, v25, v69
	v_max_f32_e32 v18, 0, v18
	v_max_f32_e32 v19, 0, v19
	v_add_f32_e32 v20, v20, v68
	v_add_f32_e32 v21, v21, v69
	v_max_f32_e32 v14, 0, v14
	v_max_f32_e32 v15, 0, v15
	v_add_f32_e32 v16, v16, v68
	v_add_f32_e32 v17, v17, v69
	v_max_f32_e32 v10, 0, v10
	v_max_f32_e32 v11, 0, v11
	v_add_f32_e32 v12, v12, v68
	v_add_f32_e32 v13, v13, v69
	v_max_f32_e32 v6, 0, v6
	v_max_f32_e32 v7, 0, v7
	v_add_f32_e32 v8, v8, v68
	v_add_f32_e32 v9, v9, v69
	v_max_f32_e32 v3, 0, v3
	v_add_f32_e32 v4, v4, v68
	v_add_f32_e32 v5, v5, v69
	v_cvt_pk_bf16_f32 v2, v2, v3
	ds_write_b64 v32, v[30:31]
	ds_write_b64 v28, v[26:27] offset:8192
	v_max_f32_e32 v24, 0, v24
	v_max_f32_e32 v25, 0, v25
	v_cvt_pk_bf16_f32 v22, v22, v23
	v_cvt_pk_bf16_f32 v23, v24, v25
	ds_write_b64 v32, v[22:23] offset:16384
	v_max_f32_e32 v20, 0, v20
	v_max_f32_e32 v21, 0, v21
	v_cvt_pk_bf16_f32 v18, v18, v19
	v_cvt_pk_bf16_f32 v19, v20, v21
	ds_write_b64 v28, v[18:19] offset:24576
	v_max_f32_e32 v16, 0, v16
	v_max_f32_e32 v17, 0, v17
	v_cvt_pk_bf16_f32 v14, v14, v15
	v_cvt_pk_bf16_f32 v15, v16, v17
	ds_write_b64 v32, v[14:15] offset:32768
	v_max_f32_e32 v12, 0, v12
	v_max_f32_e32 v13, 0, v13
	v_cvt_pk_bf16_f32 v10, v10, v11
	v_cvt_pk_bf16_f32 v11, v12, v13
	ds_write_b64 v28, v[10:11] offset:40960
	v_max_f32_e32 v8, 0, v8
	v_max_f32_e32 v9, 0, v9
	v_cvt_pk_bf16_f32 v6, v6, v7
	v_cvt_pk_bf16_f32 v7, v8, v9
	ds_write_b64 v32, v[6:7] offset:49152
	v_max_f32_e32 v4, 0, v4
	v_max_f32_e32 v5, 0, v5
	v_cvt_pk_bf16_f32 v3, v4, v5
	ds_write_b64 v28, v[2:3] offset:57344
	v_and_b32_e32 v2, 0x1f0, v1
	v_lshrrev_b32_e32 v1, 5, v0
	v_xor_b32_e32 v4, v1, v0
	v_mov_b32_e32 v3, 0
	v_lshlrev_b32_e32 v4, 4, v4
	v_lshl_add_u64 v[12:13], s[4:5], 0, v[2:3]
	v_lshlrev_b32_e32 v2, 9, v1
	v_and_b32_e32 v16, 0x1f0, v4
	v_add3_u32 v2, 0, v2, v16
	s_waitcnt lgkmcnt(0)
	s_barrier
	ds_read_b128 v[4:7], v2
	v_lshlrev_b32_e32 v2, 11, v1
	v_lshl_add_u64 v[14:15], v[12:13], 0, v[2:3]
	v_or_b32_e32 v2, 0x200, v0
	v_lshrrev_b32_e32 v2, 5, v2
	v_xor_b32_e32 v9, v2, v0
	v_lshlrev_b32_e32 v9, 4, v9
	v_lshlrev_b32_e32 v8, 9, v2
	v_and_b32_e32 v9, 0x1f0, v9
	v_add3_u32 v8, 0, v8, v9
	ds_read_b128 v[8:11], v8
	v_lshlrev_b32_e32 v2, 11, v2
	s_waitcnt lgkmcnt(1)
	global_store_dwordx4 v[14:15], v[4:7], off sc1
	s_nop 1
	v_lshl_add_u64 v[4:5], v[12:13], 0, v[2:3]
	s_waitcnt lgkmcnt(0)
	global_store_dwordx4 v[4:5], v[8:11], off sc1
	v_or_b32_e32 v2, 32, v1
	v_lshlrev_b32_e32 v4, 9, v2
	v_or_b32_e32 v8, 0x600, v0
	v_lshrrev_b32_e32 v17, 5, v8
	v_xor_b32_e32 v9, v17, v0
	v_lshlrev_b32_e32 v9, 4, v9
	v_add3_u32 v4, 0, v4, v16
	v_lshlrev_b32_e32 v8, 9, v17
	v_and_b32_e32 v9, 0x1f0, v9
	ds_read_b128 v[4:7], v4
	v_add3_u32 v8, 0, v8, v9
	ds_read_b128 v[8:11], v8
	v_lshlrev_b32_e32 v2, 11, v2
	v_lshl_add_u64 v[14:15], v[12:13], 0, v[2:3]
	v_lshlrev_b32_e32 v2, 11, v17
	s_waitcnt lgkmcnt(1)
	global_store_dwordx4 v[14:15], v[4:7], off sc1
	s_nop 1
	v_lshl_add_u64 v[4:5], v[12:13], 0, v[2:3]
	s_waitcnt lgkmcnt(0)
	global_store_dwordx4 v[4:5], v[8:11], off sc1
	v_or_b32_e32 v2, 64, v1
	v_lshlrev_b32_e32 v4, 9, v2
	v_or_b32_e32 v8, 0xa00, v0
	v_lshrrev_b32_e32 v17, 5, v8
	v_xor_b32_e32 v9, v17, v0
	v_lshlrev_b32_e32 v9, 4, v9
	v_add3_u32 v4, 0, v4, v16
	v_lshlrev_b32_e32 v8, 9, v17
	v_and_b32_e32 v9, 0x1f0, v9
	ds_read_b128 v[4:7], v4
	v_add3_u32 v8, 0, v8, v9
	ds_read_b128 v[8:11], v8
	v_lshlrev_b32_e32 v2, 11, v2
	v_lshl_add_u64 v[14:15], v[12:13], 0, v[2:3]
	v_lshlrev_b32_e32 v2, 11, v17
	s_waitcnt lgkmcnt(1)
	global_store_dwordx4 v[14:15], v[4:7], off sc1
	s_nop 1
	v_lshl_add_u64 v[4:5], v[12:13], 0, v[2:3]
	s_waitcnt lgkmcnt(0)
	global_store_dwordx4 v[4:5], v[8:11], off sc1
	v_or_b32_e32 v2, 0x60, v1
	v_lshlrev_b32_e32 v4, 9, v2
	v_or_b32_e32 v8, 0xe00, v0
	v_lshrrev_b32_e32 v17, 5, v8
	v_xor_b32_e32 v9, v17, v0
	v_lshlrev_b32_e32 v9, 4, v9
	v_add3_u32 v4, 0, v4, v16
	v_lshlrev_b32_e32 v8, 9, v17
	v_and_b32_e32 v9, 0x1f0, v9
	ds_read_b128 v[4:7], v4
	v_add3_u32 v8, 0, v8, v9
	ds_read_b128 v[8:11], v8
	v_lshlrev_b32_e32 v2, 11, v2
	v_lshl_add_u64 v[14:15], v[12:13], 0, v[2:3]
	v_lshlrev_b32_e32 v2, 11, v17
	s_waitcnt lgkmcnt(1)
	global_store_dwordx4 v[14:15], v[4:7], off sc1
	s_nop 1
	v_lshl_add_u64 v[4:5], v[12:13], 0, v[2:3]
	s_waitcnt lgkmcnt(0)
	global_store_dwordx4 v[4:5], v[8:11], off sc1
	v_or_b32_e32 v2, 0x80, v1
	v_lshlrev_b32_e32 v4, 9, v2
	v_or_b32_e32 v8, 0x1200, v0
	v_lshrrev_b32_e32 v17, 5, v8
	v_xor_b32_e32 v9, v17, v0
	v_lshlrev_b32_e32 v9, 4, v9
	v_add3_u32 v4, 0, v4, v16
	v_lshlrev_b32_e32 v8, 9, v17
	v_and_b32_e32 v9, 0x1f0, v9
	ds_read_b128 v[4:7], v4
	v_add3_u32 v8, 0, v8, v9
	ds_read_b128 v[8:11], v8
	v_lshlrev_b32_e32 v2, 11, v2
	v_lshl_add_u64 v[14:15], v[12:13], 0, v[2:3]
	v_lshlrev_b32_e32 v2, 11, v17
	s_waitcnt lgkmcnt(1)
	global_store_dwordx4 v[14:15], v[4:7], off sc1
	s_nop 1
	v_lshl_add_u64 v[4:5], v[12:13], 0, v[2:3]
	s_waitcnt lgkmcnt(0)
	global_store_dwordx4 v[4:5], v[8:11], off sc1
	v_or_b32_e32 v2, 0xa0, v1
	v_lshlrev_b32_e32 v4, 9, v2
	v_or_b32_e32 v8, 0x1600, v0
	v_lshrrev_b32_e32 v17, 5, v8
	v_xor_b32_e32 v9, v17, v0
	v_lshlrev_b32_e32 v9, 4, v9
	v_add3_u32 v4, 0, v4, v16
	v_lshlrev_b32_e32 v8, 9, v17
	v_and_b32_e32 v9, 0x1f0, v9
	ds_read_b128 v[4:7], v4
	v_add3_u32 v8, 0, v8, v9
	ds_read_b128 v[8:11], v8
	v_lshlrev_b32_e32 v2, 11, v2
	v_lshl_add_u64 v[14:15], v[12:13], 0, v[2:3]
	v_lshlrev_b32_e32 v2, 11, v17
	s_waitcnt lgkmcnt(1)
	global_store_dwordx4 v[14:15], v[4:7], off sc1
	s_nop 1
	v_lshl_add_u64 v[4:5], v[12:13], 0, v[2:3]
	s_waitcnt lgkmcnt(0)
	global_store_dwordx4 v[4:5], v[8:11], off sc1
	v_or_b32_e32 v2, 0xc0, v1
	v_lshlrev_b32_e32 v4, 9, v2
	v_or_b32_e32 v8, 0x1a00, v0
	v_lshrrev_b32_e32 v17, 5, v8
	v_xor_b32_e32 v9, v17, v0
	v_add3_u32 v4, 0, v4, v16
	v_lshlrev_b32_e32 v9, 4, v9
	ds_read_b128 v[4:7], v4
	v_lshlrev_b32_e32 v8, 9, v17
	v_and_b32_e32 v9, 0x1f0, v9
	v_add3_u32 v8, 0, v8, v9
	ds_read_b128 v[8:11], v8
	v_lshlrev_b32_e32 v2, 11, v2
	v_lshl_add_u64 v[14:15], v[12:13], 0, v[2:3]
	v_lshlrev_b32_e32 v2, 11, v17
	v_or_b32_e32 v1, 0xe0, v1
	s_waitcnt lgkmcnt(1)
	global_store_dwordx4 v[14:15], v[4:7], off sc1
	s_nop 1
	v_lshl_add_u64 v[4:5], v[12:13], 0, v[2:3]
	v_lshlrev_b32_e32 v2, 9, v1
	v_add3_u32 v2, 0, v2, v16
	s_waitcnt lgkmcnt(0)
	global_store_dwordx4 v[4:5], v[8:11], off sc1
	ds_read_b128 v[4:7], v2
	v_lshlrev_b32_e32 v2, 11, v1
	v_or_b32_e32 v1, 0x1e00, v0
	v_lshrrev_b32_e32 v1, 5, v1
	v_xor_b32_e32 v9, v1, v0
	v_lshlrev_b32_e32 v9, 4, v9
	v_lshlrev_b32_e32 v8, 9, v1
	v_and_b32_e32 v9, 0x1f0, v9
	v_add3_u32 v8, 0, v8, v9
	ds_read_b128 v[8:11], v8
	v_lshl_add_u64 v[14:15], v[12:13], 0, v[2:3]
	v_lshlrev_b32_e32 v2, 11, v1
	s_waitcnt lgkmcnt(1)
	global_store_dwordx4 v[14:15], v[4:7], off sc1
	s_nop 1
	v_lshl_add_u64 v[4:5], v[12:13], 0, v[2:3]
	s_waitcnt lgkmcnt(0)
	global_store_dwordx4 v[4:5], v[8:11], off sc1
	s_waitcnt lgkmcnt(0)
	s_barrier
	s_lshl_b32 s3, s2, 3
	s_and_b32 s3, s3, 56
	s_ashr_i32 s17, s2, 5
	s_add_i32 s20, s3, s17
	s_ashr_i32 s21, s20, 31
	s_bfe_u32 s16, s2, 0x20003
	s_lshl_b64 s[4:5], s[20:21], 17
	s_lshl_b64 s[6:7], s[20:21], 19
	s_add_u32 s6, s12, s6
	s_addc_u32 s7, s13, s7
	s_lshl_b32 s3, s16, 19
	s_add_u32 s3, s14, s3
	v_ashrrev_i32_e32 v2, 6, v0
	v_lshlrev_b32_e32 v1, 4, v0
	s_addc_u32 s13, s15, 0
	v_lshlrev_b32_e32 v4, 9, v2
	v_and_b32_e32 v5, 0x1f0, v1
	s_add_u32 s12, s3, 0x400000
	v_and_or_b32 v32, v4, s0, v5
	v_lshlrev_b32_e32 v4, 5, v2
	v_and_b32_e32 v5, 48, v1
	s_addc_u32 s13, s13, 0
	v_bitop3_b32 v4, v4, v5, 32 bitop3:0x6c
	s_and_b32 s15, s2, 8
	s_add_i32 s3, s20, 3
	v_bfe_u32 v31, v0, 5, 1
	v_lshrrev_b32_e32 v34, 1, v4
	v_add_u32_e32 v4, s15, v2
	s_mov_b32 s20, 0x3ffffe
	v_and_or_b32 v30, v4, s20, v31
	v_bfe_i32 v5, v30, 0, 22
	v_bfe_u32 v4, v30, 21, 1
	v_add_u32_e32 v6, v5, v4
	v_lshlrev_b32_e32 v4, 3, v6
	v_and_b32_e32 v6, 0x7fffffe, v6
	s_lshl_b32 s0, s17, 4
	v_sub_u32_e32 v5, v5, v6
	s_and_b32 s17, s0, 16
	v_lshl_or_b32 v6, v5, 5, v34
	v_add_u32_e32 v5, s17, v2
	v_and_or_b32 v35, v5, s20, v31
	v_bfe_i32 v7, v35, 0, 22
	v_bfe_u32 v8, v35, 21, 1
	v_add_u32_e32 v8, v7, v8
	v_lshlrev_b32_e32 v9, 3, v8
	v_and_b32_e32 v8, 0x7fffffe, v8
	v_add_u32_e32 v5, 8, v5
	v_sub_u32_e32 v7, v7, v8
	v_and_or_b32 v36, v5, s20, v31
	v_lshl_or_b32 v98, v7, 5, v34
	v_bfe_i32 v5, v36, 0, 22
	v_bfe_u32 v7, v36, 21, 1
	v_add_u32_e32 v7, v5, v7
	v_lshrrev_b32_e32 v33, 6, v32
	v_lshlrev_b32_e32 v8, 3, v7
	v_and_b32_e32 v7, 0x7fffffe, v7
	s_and_b32 s3, s3, 15
	v_and_or_b32 v4, v4, -16, v33
	v_sub_u32_e32 v5, v5, v7
	v_and_or_b32 v14, v9, -16, v33
	v_lshl_or_b32 v100, v5, 5, v34
	v_ashrrev_i32_e32 v5, 31, v4
	s_lshl_b32 s14, s3, 6
	s_lshl_b32 s0, s3, 8
	s_lshl_b32 s2, s3, 7
	v_and_or_b32 v16, v8, -16, v33
	v_lshlrev_b64 v[4:5], 12, v[4:5]
	s_add_u32 s2, s12, s2
	v_ashrrev_i32_e32 v15, 31, v14
	v_lshl_add_u64 v[4:5], s[6:7], 0, v[4:5]
	v_ashrrev_i32_e32 v7, 31, v6
	s_addc_u32 s3, s13, 0
	v_lshlrev_b64 v[102:103], 11, v[14:15]
	v_ashrrev_i32_e32 v99, 31, v98
	v_ashrrev_i32_e32 v17, 31, v16
	v_lshl_add_u64 v[8:9], v[4:5], 0, s[0:1]
	v_lshlrev_b64 v[38:39], 2, v[6:7]
	v_lshl_add_u64 v[14:15], s[2:3], 0, v[102:103]
	v_lshlrev_b64 v[22:23], 1, v[98:99]
	v_lshlrev_b64 v[104:105], 11, v[16:17]
	v_ashrrev_i32_e32 v101, 31, v100
	v_lshl_add_u64 v[18:19], v[8:9], 0, v[38:39]
	v_lshl_add_u64 v[24:25], v[14:15], 0, v[22:23]
	v_lshl_add_u64 v[14:15], s[2:3], 0, v[104:105]
	v_lshlrev_b64 v[26:27], 1, v[100:101]
	global_load_dwordx4 v[6:9], v[18:19], off offset:16
	global_load_dwordx4 v[10:13], v[18:19], off
	v_lshl_add_u64 v[28:29], v[14:15], 0, v[26:27]
	global_load_dwordx4 v[14:17], v[24:25], off
	global_load_dwordx4 v[18:21], v[28:29], off
	v_lshlrev_b32_e32 v24, 10, v30
	v_or_b32_e32 v125, v24, v32
	v_xad_u32 v24, s15, 8, v2
	v_and_or_b32 v24, v24, s20, v31
	v_lshlrev_b32_e32 v25, 10, v24
	v_or_b32_e32 v122, v25, v32
	v_bfe_i32 v25, v24, 0, 22
	v_bfe_u32 v24, v24, 21, 1
	v_add_u32_e32 v28, v25, v24
	v_lshlrev_b32_e32 v24, 3, v28
	v_and_b32_e32 v28, 0x7fffffe, v28
	v_sub_u32_e32 v25, v25, v28
	v_lshl_or_b32 v28, v25, 5, v34
	v_lshlrev_b32_e32 v25, 10, v35
	v_or_b32_e32 v126, v25, v32
	v_lshlrev_b32_e32 v25, 10, v36
	v_or_b32_e32 v127, v25, v32
	v_xad_u32 v25, s17, 16, v2
	v_and_or_b32 v25, v25, s20, v31
	v_lshlrev_b32_e32 v29, 10, v25
	v_or_b32_e32 v123, v29, v32
	v_bfe_i32 v29, v25, 0, 22
	v_bfe_u32 v25, v25, 21, 1
	v_add_u32_e32 v25, v29, v25
	v_and_b32_e32 v121, 3, v2
	v_lshlrev_b32_e32 v30, 3, v25
	v_and_b32_e32 v25, 0x7fffffe, v25
	v_xad_u32 v2, s17, 24, v2
	v_sub_u32_e32 v25, v29, v25
	v_and_or_b32 v2, v2, s20, v31
	v_lshl_or_b32 v106, v25, 5, v34
	v_lshlrev_b32_e32 v25, 10, v2
	v_or_b32_e32 v124, v25, v32
	v_bfe_i32 v25, v2, 0, 22
	v_bfe_u32 v2, v2, 21, 1
	v_add_u32_e32 v2, v25, v2
	v_lshlrev_b32_e32 v29, 3, v2
	v_and_b32_e32 v2, 0x7fffffe, v2
	v_and_b32_e32 v118, 15, v0
	v_sub_u32_e32 v2, v25, v2
	v_lshlrev_b32_e32 v25, 2, v0
	v_ashrrev_i32_e32 v120, 8, v0
	v_and_or_b32 v32, v29, -16, v33
	v_lshl_or_b32 v108, v2, 5, v34
	v_and_b32_e32 v2, 48, v0
	v_and_b32_e32 v25, 32, v25
	v_lshlrev_b32_e32 v29, 6, v118
	v_and_b32_e32 v119, 63, v0
	v_and_or_b32 v24, v24, -16, v33
	v_and_or_b32 v30, v30, -16, v33
	v_lshlrev_b32_e32 v68, 13, v120
	v_bitop3_b32 v2, v29, v25, v2 bitop3:0x36
	v_ashrrev_i32_e32 v25, 31, v24
	v_lshlrev_b64 v[24:25], 12, v[24:25]
	v_lshl_add_u64 v[56:57], s[6:7], 0, v[24:25]
	v_ashrrev_i32_e32 v29, 31, v28
	v_lshl_add_u64 v[24:25], v[56:57], 0, s[0:1]
	v_lshlrev_b64 v[58:59], 2, v[28:29]
	v_ashrrev_i32_e32 v31, 31, v30
	v_lshl_add_u64 v[24:25], v[24:25], 0, v[58:59]
	v_lshlrev_b64 v[110:111], 11, v[30:31]
	v_ashrrev_i32_e32 v107, 31, v106
	v_ashrrev_i32_e32 v33, 31, v32
	global_load_dwordx4 v[40:43], v[24:25], off offset:16
	global_load_dwordx4 v[44:47], v[24:25], off
	v_lshl_add_u64 v[24:25], s[2:3], 0, v[110:111]
	v_lshlrev_b64 v[60:61], 1, v[106:107]
	v_lshlrev_b64 v[112:113], 11, v[32:33]
	v_ashrrev_i32_e32 v109, 31, v108
	v_lshl_add_u64 v[24:25], v[24:25], 0, v[60:61]
	v_lshl_add_u64 v[28:29], s[2:3], 0, v[112:113]
	v_lshlrev_b64 v[62:63], 1, v[108:109]
	v_lshl_add_u64 v[28:29], v[28:29], 0, v[62:63]
	global_load_dwordx4 v[48:51], v[24:25], off
	global_load_dwordx4 v[52:55], v[28:29], off
	s_add_i32 s0, s14, 64
	s_and_b32 s2, s0, 0x3c0
	s_lshl_b32 s0, s2, 2
	s_lshl_b32 s2, s2, 1
	v_lshl_add_u64 v[24:25], v[4:5], 0, s[0:1]
	s_add_u32 s2, s12, s2
	v_lshl_add_u64 v[24:25], v[24:25], 0, v[38:39]
	s_addc_u32 s3, s13, 0
	global_load_dwordx4 v[30:33], v[24:25], off offset:16
	global_load_dwordx4 v[34:37], v[24:25], off
	v_lshl_add_u64 v[24:25], s[2:3], 0, v[102:103]
	v_lshl_add_u64 v[64:65], v[24:25], 0, v[22:23]
	v_lshl_add_u64 v[22:23], s[2:3], 0, v[104:105]
	v_lshl_add_u64 v[66:67], v[22:23], 0, v[26:27]
	global_load_dwordx4 v[26:29], v[64:65], off
	global_load_dwordx4 v[22:25], v[66:67], off
	v_add_u32_e32 v64, 0, v125
	s_waitcnt vmcnt(10)
	v_cvt_pk_bf16_f32 v10, v10, v11
	v_cvt_pk_bf16_f32 v11, v12, v13
	v_cvt_pk_bf16_f32 v12, v6, v7
	v_add_u32_e32 v6, 0, v126
	v_cvt_pk_bf16_f32 v13, v8, v9
	ds_write_b128 v64, v[10:13]
	s_waitcnt vmcnt(9)
	ds_write_b128 v6, v[14:17] offset:32768
	v_add_u32_e32 v6, 0, v127
	s_waitcnt vmcnt(8)
	ds_write_b128 v6, v[18:21] offset:32768
	v_add_u32_e32 v10, 0, v122
	s_waitcnt vmcnt(6)
	v_cvt_pk_bf16_f32 v6, v44, v45
	v_cvt_pk_bf16_f32 v7, v46, v47
	v_cvt_pk_bf16_f32 v8, v40, v41
	v_cvt_pk_bf16_f32 v9, v42, v43
	ds_write_b128 v10, v[6:9]
	v_add_u32_e32 v6, 0, v123
	s_waitcnt vmcnt(5)
	ds_write_b128 v6, v[48:51] offset:32768
	v_add_u32_e32 v6, 0, v124
	s_waitcnt vmcnt(4)
	ds_write_b128 v6, v[52:55] offset:32768
	v_lshl_add_u64 v[6:7], v[56:57], 0, s[0:1]
	v_lshl_add_u64 v[14:15], v[6:7], 0, v[58:59]
	global_load_dwordx4 v[6:9], v[14:15], off offset:16
	global_load_dwordx4 v[10:13], v[14:15], off
	v_lshl_add_u64 v[14:15], s[2:3], 0, v[110:111]
	v_lshl_add_u64 v[40:41], v[14:15], 0, v[60:61]
	v_lshl_add_u64 v[14:15], s[2:3], 0, v[112:113]
	v_lshl_add_u64 v[42:43], v[14:15], 0, v[62:63]
	global_load_dwordx4 v[18:21], v[40:41], off
	global_load_dwordx4 v[14:17], v[42:43], off
	v_lshlrev_b32_e32 v40, 13, v121
	s_cmp_lg_u32 0, -1
	s_waitcnt lgkmcnt(0)
	s_cselect_b32 s0, 0, 0
	v_add3_u32 v128, v68, s0, v2
	s_add_i32 s0, s0, 0x8000
	v_add3_u32 v129, v40, s0, v2
	v_lshl_add_u64 v[114:115], v[4:5], 0, v[38:39]
	v_lshl_add_u64 v[116:117], v[56:57], 0, v[58:59]
	s_add_i32 s2, s14, 0x80
	s_mov_b32 s3, 0
	v_mov_b32_e32 v2, v3
	v_mov_b32_e32 v4, v3
	v_mov_b32_e32 v5, v3
	v_mov_b32_e32 v38, v3
	v_mov_b32_e32 v39, v3
	v_mov_b32_e32 v40, v3
	v_mov_b32_e32 v41, v3
	v_mov_b32_e32 v42, v3
	v_mov_b32_e32 v43, v3
	v_mov_b32_e32 v44, v3
	v_mov_b32_e32 v45, v3
	v_mov_b32_e32 v46, v3
	v_mov_b32_e32 v47, v3
	v_mov_b32_e32 v48, v3
	v_mov_b32_e32 v49, v3
	v_mov_b32_e32 v50, v3
	v_mov_b32_e32 v51, v3
	v_mov_b32_e32 v52, v3
	v_mov_b32_e32 v53, v3
	v_mov_b32_e32 v54, v3
	v_mov_b32_e32 v55, v3
	v_mov_b32_e32 v56, v3
	v_mov_b32_e32 v57, v3
	v_mov_b32_e32 v58, v3
	v_mov_b32_e32 v59, v3
	v_mov_b32_e32 v60, v3
	v_mov_b32_e32 v61, v3
	v_mov_b32_e32 v62, v3
	v_mov_b32_e32 v63, v3
	v_mov_b32_e32 v64, v3
	v_mov_b32_e32 v65, v3
	v_mov_b32_e32 v66, v3
	v_mov_b32_e32 v67, v3
	v_mov_b32_e32 v68, v3
	v_mov_b32_e32 v69, v3
	v_mov_b32_e32 v70, v3
	v_mov_b32_e32 v71, v3
	v_mov_b32_e32 v72, v3
	v_mov_b32_e32 v73, v3
	v_mov_b32_e32 v74, v3
	v_mov_b32_e32 v75, v3
	v_mov_b32_e32 v76, v3
	v_mov_b32_e32 v77, v3
	v_mov_b32_e32 v78, v3
	v_mov_b32_e32 v79, v3
	v_mov_b32_e32 v80, v3
	v_mov_b32_e32 v81, v3
	v_mov_b32_e32 v82, v3
	v_mov_b32_e32 v83, v3
	v_mov_b32_e32 v84, v3
	v_mov_b32_e32 v85, v3
	v_mov_b32_e32 v86, v3
	v_mov_b32_e32 v87, v3
	v_mov_b32_e32 v88, v3
	v_mov_b32_e32 v89, v3
	v_mov_b32_e32 v90, v3
	v_mov_b32_e32 v91, v3
	v_mov_b32_e32 v92, v3
	v_mov_b32_e32 v93, v3
	v_mov_b32_e32 v94, v3
	v_mov_b32_e32 v95, v3
	v_mov_b32_e32 v96, v3
	v_mov_b32_e32 v97, v3
	s_barrier
.LBB1_3:
	s_and_b32 s0, s3, 0x10000
	v_add_u32_e32 v158, s0, v128
	v_add_u32_e32 v159, s0, v129
	ds_read_b128 v[130:133], v159 offset:0
	ds_read_b128 v[134:137], v159 offset:2048
	ds_read_b128 v[138:141], v159 offset:4096
	ds_read_b128 v[142:145], v159 offset:6144
	ds_read_b128 v[146:149], v158 offset:0
	ds_read_b128 v[150:153], v158 offset:2048
	ds_read_b128 v[154:157], v158 offset:4096
	ds_read_b128 v[160:163], v158 offset:6144
	s_waitcnt lgkmcnt(2)
	v_mfma_f32_16x16x32_bf16 v[94:97], v[130:133], v[146:149], v[94:97]
	v_mfma_f32_16x16x32_bf16 v[90:93], v[134:137], v[146:149], v[90:93]
	v_mfma_f32_16x16x32_bf16 v[86:89], v[138:141], v[146:149], v[86:89]
	v_mfma_f32_16x16x32_bf16 v[82:85], v[142:145], v[146:149], v[82:85]
	v_mfma_f32_16x16x32_bf16 v[78:81], v[130:133], v[150:153], v[78:81]
	v_mfma_f32_16x16x32_bf16 v[74:77], v[134:137], v[150:153], v[74:77]
	v_mfma_f32_16x16x32_bf16 v[70:73], v[138:141], v[150:153], v[70:73]
	v_mfma_f32_16x16x32_bf16 v[66:69], v[142:145], v[150:153], v[66:69]
	s_waitcnt lgkmcnt(0)
	v_mfma_f32_16x16x32_bf16 v[62:65], v[130:133], v[154:157], v[62:65]
	v_mfma_f32_16x16x32_bf16 v[58:61], v[134:137], v[154:157], v[58:61]
	v_mfma_f32_16x16x32_bf16 v[54:57], v[138:141], v[154:157], v[54:57]
	v_mfma_f32_16x16x32_bf16 v[50:53], v[142:145], v[154:157], v[50:53]
	v_mfma_f32_16x16x32_bf16 v[46:49], v[130:133], v[160:163], v[46:49]
	v_mfma_f32_16x16x32_bf16 v[42:45], v[134:137], v[160:163], v[42:45]
	v_mfma_f32_16x16x32_bf16 v[38:41], v[138:141], v[160:163], v[38:41]
	v_mfma_f32_16x16x32_bf16 v[2:5], v[142:145], v[160:163], v[2:5]
	s_xor_b32 s0, s0, 0x10000
	s_and_b32 s6, s2, 0x3c0
	s_add_i32 s14, s0, 0
	s_lshl_b32 s0, s6, 2
	s_lshl_b32 s6, s6, 1
	s_add_u32 s6, s12, s6
	s_waitcnt vmcnt(6)
	v_cvt_pk_bf16_f32 v34, v34, v35
	v_cvt_pk_bf16_f32 v35, v36, v37
	v_cvt_pk_bf16_f32 v36, v30, v31
	v_cvt_pk_bf16_f32 v37, v32, v33
	v_add_u32_e32 v30, s14, v125
	s_addc_u32 s7, s13, 0
	v_add_u32_e32 v31, s14, v126
	v_add_u32_e32 v32, s14, v127
	ds_write_b128 v30, v[34:37]
	s_waitcnt vmcnt(5)
	ds_write_b128 v31, v[26:29] offset:32768
	s_waitcnt vmcnt(4)
	ds_write_b128 v32, v[22:25] offset:32768
	v_lshl_add_u64 v[22:23], s[6:7], 0, v[102:103]
	v_lshl_add_u64 v[24:25], s[6:7], 0, v[104:105]
	v_lshl_add_u64 v[130:131], v[114:115], 0, s[0:1]
	v_lshl_add_u64 v[22:23], v[98:99], 1, v[22:23]
	v_lshl_add_u64 v[24:25], v[100:101], 1, v[24:25]
	global_load_dwordx4 v[30:33], v[130:131], off offset:16
	global_load_dwordx4 v[34:37], v[130:131], off
	global_load_dwordx4 v[26:29], v[22:23], off
	s_nop 0
	global_load_dwordx4 v[22:25], v[24:25], off
	ds_read_b128 v[130:133], v159 offset:1024
	ds_read_b128 v[134:137], v159 offset:3072
	ds_read_b128 v[138:141], v159 offset:5120
	ds_read_b128 v[142:145], v159 offset:7168
	ds_read_b128 v[146:149], v158 offset:1024
	ds_read_b128 v[150:153], v158 offset:3072
	ds_read_b128 v[154:157], v158 offset:5120
	ds_read_b128 v[160:163], v158 offset:7168
	s_waitcnt lgkmcnt(2)
	v_mfma_f32_16x16x32_bf16 v[94:97], v[130:133], v[146:149], v[94:97]
	v_mfma_f32_16x16x32_bf16 v[90:93], v[134:137], v[146:149], v[90:93]
	v_mfma_f32_16x16x32_bf16 v[86:89], v[138:141], v[146:149], v[86:89]
	v_mfma_f32_16x16x32_bf16 v[82:85], v[142:145], v[146:149], v[82:85]
	v_mfma_f32_16x16x32_bf16 v[78:81], v[130:133], v[150:153], v[78:81]
	v_mfma_f32_16x16x32_bf16 v[74:77], v[134:137], v[150:153], v[74:77]
	v_mfma_f32_16x16x32_bf16 v[70:73], v[138:141], v[150:153], v[70:73]
	v_mfma_f32_16x16x32_bf16 v[66:69], v[142:145], v[150:153], v[66:69]
	s_waitcnt lgkmcnt(0)
	v_mfma_f32_16x16x32_bf16 v[62:65], v[130:133], v[154:157], v[62:65]
	v_mfma_f32_16x16x32_bf16 v[58:61], v[134:137], v[154:157], v[58:61]
	v_mfma_f32_16x16x32_bf16 v[54:57], v[138:141], v[154:157], v[54:57]
	v_mfma_f32_16x16x32_bf16 v[50:53], v[142:145], v[154:157], v[50:53]
	v_mfma_f32_16x16x32_bf16 v[46:49], v[130:133], v[160:163], v[46:49]
	v_mfma_f32_16x16x32_bf16 v[42:45], v[134:137], v[160:163], v[42:45]
	v_mfma_f32_16x16x32_bf16 v[38:41], v[138:141], v[160:163], v[38:41]
	v_mfma_f32_16x16x32_bf16 v[2:5], v[142:145], v[160:163], v[2:5]
	v_add_u32_e32 v130, s14, v122
	s_waitcnt vmcnt(6)
	v_cvt_pk_bf16_f32 v10, v10, v11
	v_cvt_pk_bf16_f32 v11, v12, v13
	v_cvt_pk_bf16_f32 v12, v6, v7
	v_add_u32_e32 v6, s14, v123
	v_cvt_pk_bf16_f32 v13, v8, v9
	ds_write_b128 v130, v[10:13]
	s_waitcnt vmcnt(5)
	ds_write_b128 v6, v[18:21] offset:32768
	v_add_u32_e32 v6, s14, v124
	s_waitcnt vmcnt(4)
	ds_write_b128 v6, v[14:17] offset:32768
	v_lshl_add_u64 v[14:15], s[6:7], 0, v[110:111]
	v_lshl_add_u64 v[16:17], s[6:7], 0, v[112:113]
	v_lshl_add_u64 v[10:11], v[116:117], 0, s[0:1]
	v_lshl_add_u64 v[14:15], v[106:107], 1, v[14:15]
	v_lshl_add_u64 v[16:17], v[108:109], 1, v[16:17]
	global_load_dwordx4 v[6:9], v[10:11], off offset:16
	s_nop 0
	global_load_dwordx4 v[10:13], v[10:11], off
	s_nop 0
	global_load_dwordx4 v[18:21], v[14:15], off
	s_nop 0
	global_load_dwordx4 v[14:17], v[16:17], off
	s_waitcnt lgkmcnt(0)
	s_add_i32 s2, s2, 64
	s_add_i32 s3, s3, 0x10000
	s_cmp_lg_u32 s3, 0xe0000
	s_barrier
	s_cbranch_scc1 .LBB1_3
	ds_read_b128 v[98:101], v129 offset:0
	ds_read_b128 v[102:105], v129 offset:0x800
	ds_read_b128 v[106:109], v129 offset:0x1000
	ds_read_b128 v[110:113], v129 offset:0x1800
	ds_read_b128 v[114:117], v128 offset:0
	ds_read_b128 v[130:133], v128 offset:0x800
	ds_read_b128 v[134:137], v128 offset:0x1000
	s_waitcnt lgkmcnt(2)
	v_mfma_f32_16x16x32_bf16 v[94:97], v[98:101], v[114:117], v[94:97]
	v_mfma_f32_16x16x32_bf16 v[90:93], v[102:105], v[114:117], v[90:93]
	v_mfma_f32_16x16x32_bf16 v[86:89], v[106:109], v[114:117], v[86:89]
	v_mfma_f32_16x16x32_bf16 v[82:85], v[110:113], v[114:117], v[82:85]
	ds_read_b128 v[114:117], v128 offset:0x1800
	s_waitcnt lgkmcnt(2)
	v_mfma_f32_16x16x32_bf16 v[78:81], v[98:101], v[130:133], v[78:81]
	v_mfma_f32_16x16x32_bf16 v[74:77], v[102:105], v[130:133], v[74:77]
	v_mfma_f32_16x16x32_bf16 v[70:73], v[106:109], v[130:133], v[70:73]
	v_mfma_f32_16x16x32_bf16 v[66:69], v[110:113], v[130:133], v[66:69]
	s_waitcnt lgkmcnt(1)
	v_mfma_f32_16x16x32_bf16 v[62:65], v[98:101], v[134:137], v[62:65]
	v_mfma_f32_16x16x32_bf16 v[58:61], v[102:105], v[134:137], v[58:61]
	v_mfma_f32_16x16x32_bf16 v[54:57], v[106:109], v[134:137], v[54:57]
	v_mfma_f32_16x16x32_bf16 v[50:53], v[110:113], v[134:137], v[50:53]
	s_waitcnt lgkmcnt(0)
	v_mfma_f32_16x16x32_bf16 v[46:49], v[98:101], v[114:117], v[46:49]
	v_mfma_f32_16x16x32_bf16 v[42:45], v[102:105], v[114:117], v[42:45]
	v_mfma_f32_16x16x32_bf16 v[38:41], v[106:109], v[114:117], v[38:41]
	v_mfma_f32_16x16x32_bf16 v[2:5], v[110:113], v[114:117], v[2:5]
	v_add_u32_e32 v98, s18, v125
	s_waitcnt vmcnt(6)
	v_cvt_pk_bf16_f32 v34, v34, v35
	v_cvt_pk_bf16_f32 v35, v36, v37
	v_cvt_pk_bf16_f32 v36, v30, v31
	v_add_u32_e32 v30, s19, v126
	v_cvt_pk_bf16_f32 v37, v32, v33
	ds_write_b128 v98, v[34:37]
	s_waitcnt vmcnt(5)
	ds_write_b128 v30, v[26:29]
	v_add_u32_e32 v26, s19, v127
	s_waitcnt vmcnt(4)
	ds_write_b128 v26, v[22:25]
	ds_read_b128 v[22:25], v129 offset:0x400
	ds_read_b128 v[26:29], v129 offset:0xc00
	ds_read_b128 v[30:33], v129 offset:0x1400
	ds_read_b128 v[34:37], v129 offset:0x1c00
	ds_read_b128 v[98:101], v128 offset:0x400
	ds_read_b128 v[102:105], v128 offset:0xc00
	ds_read_b128 v[106:109], v128 offset:0x1400
	s_waitcnt lgkmcnt(2)
	v_mfma_f32_16x16x32_bf16 v[94:97], v[22:25], v[98:101], v[94:97]
	v_mfma_f32_16x16x32_bf16 v[90:93], v[26:29], v[98:101], v[90:93]
	v_mfma_f32_16x16x32_bf16 v[86:89], v[30:33], v[98:101], v[86:89]
	v_mfma_f32_16x16x32_bf16 v[82:85], v[34:37], v[98:101], v[82:85]
	ds_read_b128 v[98:101], v128 offset:0x1c00
	s_waitcnt lgkmcnt(2)
	v_mfma_f32_16x16x32_bf16 v[78:81], v[22:25], v[102:105], v[78:81]
	v_mfma_f32_16x16x32_bf16 v[74:77], v[26:29], v[102:105], v[74:77]
	v_mfma_f32_16x16x32_bf16 v[70:73], v[30:33], v[102:105], v[70:73]
	v_mfma_f32_16x16x32_bf16 v[66:69], v[34:37], v[102:105], v[66:69]
	s_waitcnt lgkmcnt(1)
	v_mfma_f32_16x16x32_bf16 v[62:65], v[22:25], v[106:109], v[62:65]
	v_mfma_f32_16x16x32_bf16 v[58:61], v[26:29], v[106:109], v[58:61]
	v_mfma_f32_16x16x32_bf16 v[54:57], v[30:33], v[106:109], v[54:57]
	v_mfma_f32_16x16x32_bf16 v[50:53], v[34:37], v[106:109], v[50:53]
	s_waitcnt lgkmcnt(0)
	v_mfma_f32_16x16x32_bf16 v[22:25], v[22:25], v[98:101], v[46:49]
	v_mfma_f32_16x16x32_bf16 v[26:29], v[26:29], v[98:101], v[42:45]
	v_mfma_f32_16x16x32_bf16 v[30:33], v[30:33], v[98:101], v[38:41]
	v_mfma_f32_16x16x32_bf16 v[2:5], v[34:37], v[98:101], v[2:5]
	v_add_u32_e32 v34, s18, v122
	s_waitcnt vmcnt(2)
	v_cvt_pk_bf16_f32 v10, v10, v11
	v_cvt_pk_bf16_f32 v11, v12, v13
	v_cvt_pk_bf16_f32 v12, v6, v7
	v_add_u32_e32 v6, s19, v123
	s_lshl_b64 s[0:1], s[4:5], 1
	v_cvt_pk_bf16_f32 v13, v8, v9
	ds_write_b128 v34, v[10:13]
	s_waitcnt vmcnt(1)
	ds_write_b128 v6, v[18:21]
	v_add_u32_e32 v6, s19, v124
	s_add_u32 s0, s10, s0
	s_waitcnt vmcnt(0)
	ds_write_b128 v6, v[14:17]
	s_addc_u32 s1, s11, s1
	s_lshl_b32 s2, s16, 9
	s_waitcnt lgkmcnt(0)
	s_barrier
	v_add_u32_e32 v110, 0x10000, v128
	v_add_u32_e32 v102, 0x10000, v129
	ds_read_b128 v[6:9], v102 offset:0
	ds_read_b128 v[10:13], v102 offset:0x800
	ds_read_b128 v[14:17], v102 offset:0x1000
	ds_read_b128 v[18:21], v102 offset:0x1800
	ds_read_b128 v[34:37], v110 offset:0
	ds_read_b128 v[38:41], v110 offset:0x800
	ds_read_b128 v[42:45], v110 offset:0x1000
	s_add_u32 s0, s0, s2
	s_addc_u32 s1, s1, 0
	s_lshl_b32 s2, s16, 10
	s_waitcnt lgkmcnt(2)
	s_add_u32 s2, s8, s2
	v_mfma_f32_16x16x32_bf16 v[46:49], v[6:9], v[34:37], v[94:97]
	s_addc_u32 s3, s9, 0
	v_mfma_f32_16x16x32_bf16 v[90:93], v[10:13], v[34:37], v[90:93]
	v_mfma_f32_16x16x32_bf16 v[86:89], v[14:17], v[34:37], v[86:89]
	v_mfma_f32_16x16x32_bf16 v[34:37], v[18:21], v[34:37], v[82:85]
	ds_read_b128 v[82:85], v110 offset:0x1800
	s_waitcnt lgkmcnt(2)
	v_mfma_f32_16x16x32_bf16 v[78:81], v[6:9], v[38:41], v[78:81]
	v_mfma_f32_16x16x32_bf16 v[74:77], v[10:13], v[38:41], v[74:77]
	v_mfma_f32_16x16x32_bf16 v[70:73], v[14:17], v[38:41], v[70:73]
	v_mfma_f32_16x16x32_bf16 v[38:41], v[18:21], v[38:41], v[66:69]
	s_waitcnt lgkmcnt(1)
	v_mfma_f32_16x16x32_bf16 v[62:65], v[6:9], v[42:45], v[62:65]
	v_mfma_f32_16x16x32_bf16 v[58:61], v[10:13], v[42:45], v[58:61]
	v_mfma_f32_16x16x32_bf16 v[54:57], v[14:17], v[42:45], v[54:57]
	v_mfma_f32_16x16x32_bf16 v[42:45], v[18:21], v[42:45], v[50:53]
	s_waitcnt lgkmcnt(0)
	v_mfma_f32_16x16x32_bf16 v[50:53], v[6:9], v[82:85], v[22:25]
	v_mfma_f32_16x16x32_bf16 v[66:69], v[10:13], v[82:85], v[26:29]
	v_mfma_f32_16x16x32_bf16 v[94:97], v[14:17], v[82:85], v[30:33]
	v_mfma_f32_16x16x32_bf16 v[2:5], v[18:21], v[82:85], v[2:5]
	ds_read_b128 v[18:21], v102 offset:0x400
	ds_read_b128 v[82:85], v102 offset:0xc00
	ds_read_b128 v[98:101], v102 offset:0x1400
	ds_read_b128 v[102:105], v102 offset:0x1c00
	ds_read_b128 v[6:9], v110 offset:0x400
	ds_read_b128 v[10:13], v110 offset:0xc00
	ds_read_b128 v[106:109], v110 offset:0x1400
	s_waitcnt lgkmcnt(2)
	v_mfma_f32_16x16x32_bf16 v[46:49], v[18:21], v[6:9], v[46:49]
	v_mfma_f32_16x16x32_bf16 v[90:93], v[82:85], v[6:9], v[90:93]
	v_mfma_f32_16x16x32_bf16 v[30:33], v[98:101], v[6:9], v[86:89]
	v_mfma_f32_16x16x32_bf16 v[14:17], v[102:105], v[6:9], v[34:37]
	ds_read_b128 v[86:89], v110 offset:0x1c00
	s_waitcnt lgkmcnt(2)
	v_mfma_f32_16x16x32_bf16 v[78:81], v[18:21], v[10:13], v[78:81]
	v_mfma_f32_16x16x32_bf16 v[74:77], v[82:85], v[10:13], v[74:77]
	v_mfma_f32_16x16x32_bf16 v[26:29], v[98:101], v[10:13], v[70:73]
	v_mfma_f32_16x16x32_bf16 v[10:13], v[102:105], v[10:13], v[38:41]
	s_waitcnt lgkmcnt(1)
	v_mfma_f32_16x16x32_bf16 v[62:65], v[18:21], v[106:109], v[62:65]
	v_mfma_f32_16x16x32_bf16 v[38:41], v[82:85], v[106:109], v[58:61]
	v_mfma_f32_16x16x32_bf16 v[22:25], v[98:101], v[106:109], v[54:57]
	v_mfma_f32_16x16x32_bf16 v[6:9], v[102:105], v[106:109], v[42:45]
	s_waitcnt lgkmcnt(0)
	v_mfma_f32_16x16x32_bf16 v[42:45], v[18:21], v[86:89], v[50:53]
	v_mfma_f32_16x16x32_bf16 v[34:37], v[82:85], v[86:89], v[66:69]
	v_mfma_f32_16x16x32_bf16 v[18:21], v[98:101], v[86:89], v[94:97]
	v_mfma_f32_16x16x32_bf16 v[2:5], v[102:105], v[86:89], v[2:5]
	v_lshrrev_b32_e32 v50, 2, v119
	v_and_b32_e32 v50, 12, v50
	v_lshl_or_b32 v66, v121, 6, v50
	v_lshlrev_b32_e32 v67, 2, v66
	s_waitcnt lgkmcnt(0)
	s_barrier
	global_load_dwordx4 v[50:53], v67, s[2:3]
	global_load_dwordx4 v[54:57], v67, s[2:3] offset:64
	v_lshrrev_b32_e32 v58, 1, v119
	v_lshl_or_b32 v59, v120, 6, v118
	v_and_b32_e32 v68, 8, v58
	v_lshl_add_u32 v69, v59, 9, 0
	v_or_b32_e32 v70, 16, v59
	v_or_b32_e32 v71, 48, v59
	v_lshrrev_b32_e32 v58, 3, v66
	v_or_b32_e32 v59, 16, v66
	v_bitop3_b32 v83, v70, v58, 31 bitop3:0x6c
	v_lshrrev_b32_e32 v85, 3, v59
	v_lshl_add_u32 v72, v70, 9, 0
	v_xor_b32_e32 v82, v58, v118
	v_bitop3_b32 v84, v71, v58, 31 bitop3:0x6c
	v_lshlrev_b32_e32 v83, 4, v83
	v_xor_b32_e32 v86, v85, v118
	v_lshl_add_u32 v73, v71, 9, 0
	v_lshlrev_b32_e32 v82, 4, v82
	v_lshlrev_b32_e32 v84, 4, v84
	v_add3_u32 v83, v72, v83, v68
	v_lshlrev_b32_e32 v86, 4, v86
	global_load_dwordx4 v[58:61], v67, s[2:3] offset:128
	v_add3_u32 v82, v69, v82, v68
	v_add3_u32 v84, v73, v84, v68
	v_add3_u32 v86, v69, v86, v68
	s_waitcnt vmcnt(2)
	v_add_f32_e32 v46, v46, v50
	v_add_f32_e32 v47, v47, v51
	v_add_f32_e32 v48, v48, v52
	v_add_f32_e32 v49, v49, v53
	v_add_f32_e32 v78, v78, v50
	v_add_f32_e32 v79, v79, v51
	v_add_f32_e32 v80, v80, v52
	v_add_f32_e32 v81, v81, v53
	v_add_f32_e32 v62, v62, v50
	v_add_f32_e32 v63, v63, v51
	v_add_f32_e32 v42, v42, v50
	v_add_f32_e32 v43, v43, v51
	v_add_f32_e32 v44, v44, v52
	v_add_f32_e32 v45, v45, v53
	s_waitcnt vmcnt(1)
	v_add_f32_e32 v50, v90, v54
	v_add_f32_e32 v51, v91, v55
	v_add_f32_e32 v64, v64, v52
	v_add_f32_e32 v65, v65, v53
	v_add_f32_e32 v52, v92, v56
	v_add_f32_e32 v53, v93, v57
	v_max_f32_e32 v46, 0, v46
	v_max_f32_e32 v47, 0, v47
	v_max_f32_e32 v48, 0, v48
	v_max_f32_e32 v49, 0, v49
	v_max_f32_e32 v78, 0, v78
	v_max_f32_e32 v79, 0, v79
	v_max_f32_e32 v80, 0, v80
	v_max_f32_e32 v81, 0, v81
	v_max_f32_e32 v88, 0, v43
	v_max_f32_e32 v89, 0, v44
	v_max_f32_e32 v90, 0, v45
	v_max_f32_e32 v50, 0, v50
	v_max_f32_e32 v51, 0, v51
	v_cvt_pk_bf16_f32 v43, v48, v49
	v_cvt_pk_bf16_f32 v44, v78, v79
	v_cvt_pk_bf16_f32 v45, v80, v81
	v_max_f32_e32 v62, 0, v62
	v_max_f32_e32 v63, 0, v63
	v_max_f32_e32 v64, 0, v64
	v_max_f32_e32 v65, 0, v65
	v_max_f32_e32 v87, 0, v42
	v_max_f32_e32 v52, 0, v52
	v_max_f32_e32 v53, 0, v53
	v_cvt_pk_bf16_f32 v42, v46, v47
	v_cvt_pk_bf16_f32 v46, v62, v63
	v_cvt_pk_bf16_f32 v47, v64, v65
	v_cvt_pk_bf16_f32 v48, v87, v88
	v_cvt_pk_bf16_f32 v49, v89, v90
	v_cvt_pk_bf16_f32 v50, v50, v51
	v_cvt_pk_bf16_f32 v51, v52, v53
	ds_write_b64 v83, v[44:45]
	ds_write2st64_b64 v82, v[42:43], v[46:47] offset1:32
	ds_write_b64 v84, v[48:49]
	ds_write_b64 v86, v[50:51]
	v_add_f32_e32 v43, v76, v56
	v_add_f32_e32 v44, v77, v57
	v_max_f32_e32 v43, 0, v43
	v_max_f32_e32 v44, 0, v44
	v_add_f32_e32 v42, v75, v55
	v_cvt_pk_bf16_f32 v43, v43, v44
	v_bitop3_b32 v44, v85, v70, 31 bitop3:0x78
	v_add_f32_e32 v74, v74, v54
	v_max_f32_e32 v42, 0, v42
	v_lshlrev_b32_e32 v44, 4, v44
	v_max_f32_e32 v74, 0, v74
	v_cvt_pk_bf16_f32 v42, v74, v42
	v_add3_u32 v44, v72, v44, v68
	ds_write_b64 v44, v[42:43]
	global_load_dwordx4 v[42:45], v67, s[2:3] offset:192
	v_add_f32_e32 v34, v34, v54
	v_add_f32_e32 v35, v35, v55
	v_add_f32_e32 v36, v36, v56
	v_max_f32_e32 v34, 0, v34
	v_max_f32_e32 v35, 0, v35
	v_max_f32_e32 v36, 0, v36
	v_add_f32_e32 v37, v37, v57
	v_max_f32_e32 v37, 0, v37
	v_cvt_pk_bf16_f32 v34, v34, v35
	v_cvt_pk_bf16_f32 v35, v36, v37
	v_bitop3_b32 v36, v85, v71, 31 bitop3:0x78
	v_add_f32_e32 v38, v38, v54
	v_add_f32_e32 v39, v39, v55
	v_lshlrev_b32_e32 v36, 4, v36
	v_max_f32_e32 v38, 0, v38
	v_max_f32_e32 v39, 0, v39
	v_add_f32_e32 v40, v40, v56
	v_add_f32_e32 v41, v41, v57
	v_add3_u32 v36, v73, v36, v68
	v_max_f32_e32 v40, 0, v40
	v_max_f32_e32 v41, 0, v41
	v_cvt_pk_bf16_f32 v38, v38, v39
	v_cvt_pk_bf16_f32 v39, v40, v41
	ds_write_b64 v86, v[38:39] offset:16384
	ds_write_b64 v36, v[34:35]
	v_or_b32_e32 v34, 32, v66
	s_waitcnt vmcnt(1)
	v_add_f32_e32 v30, v30, v58
	v_add_f32_e32 v31, v31, v59
	v_add_f32_e32 v32, v32, v60
	v_add_f32_e32 v26, v26, v58
	v_add_f32_e32 v27, v27, v59
	v_add_f32_e32 v28, v28, v60
	v_add_f32_e32 v18, v18, v58
	v_add_f32_e32 v19, v19, v59
	v_add_f32_e32 v20, v20, v60
	v_lshrrev_b32_e32 v34, 3, v34
	v_max_f32_e32 v30, 0, v30
	v_max_f32_e32 v31, 0, v31
	v_max_f32_e32 v32, 0, v32
	v_add_f32_e32 v33, v33, v61
	v_max_f32_e32 v26, 0, v26
	v_max_f32_e32 v27, 0, v27
	v_max_f32_e32 v28, 0, v28
	v_add_f32_e32 v29, v29, v61
	v_max_f32_e32 v18, 0, v18
	v_max_f32_e32 v19, 0, v19
	v_max_f32_e32 v20, 0, v20
	v_add_f32_e32 v21, v21, v61
	v_max_f32_e32 v33, 0, v33
	v_cvt_pk_bf16_f32 v30, v30, v31
	v_cvt_pk_bf16_f32 v31, v32, v33
	v_xor_b32_e32 v32, v34, v118
	v_max_f32_e32 v29, 0, v29
	v_cvt_pk_bf16_f32 v26, v26, v27
	v_cvt_pk_bf16_f32 v27, v28, v29
	v_bitop3_b32 v28, v34, v70, 31 bitop3:0x78
	v_max_f32_e32 v21, 0, v21
	v_cvt_pk_bf16_f32 v18, v18, v19
	v_cvt_pk_bf16_f32 v19, v20, v21
	v_bitop3_b32 v20, v34, v71, 31 bitop3:0x78
	v_lshlrev_b32_e32 v32, 4, v32
	v_lshlrev_b32_e32 v28, 4, v28
	v_add_f32_e32 v22, v22, v58
	v_add_f32_e32 v23, v23, v59
	v_lshlrev_b32_e32 v20, 4, v20
	v_add3_u32 v32, v69, v32, v68
	v_add3_u32 v28, v72, v28, v68
	v_max_f32_e32 v22, 0, v22
	v_max_f32_e32 v23, 0, v23
	v_add_f32_e32 v24, v24, v60
	v_add_f32_e32 v25, v25, v61
	v_add3_u32 v20, v73, v20, v68
	ds_write_b64 v32, v[30:31]
	ds_write_b64 v28, v[26:27]
	v_max_f32_e32 v24, 0, v24
	v_max_f32_e32 v25, 0, v25
	v_cvt_pk_bf16_f32 v22, v22, v23
	v_cvt_pk_bf16_f32 v23, v24, v25
	ds_write_b64 v32, v[22:23] offset:16384
	ds_write_b64 v20, v[18:19]
	v_or_b32_e32 v18, 48, v66
	s_waitcnt vmcnt(0)
	v_add_f32_e32 v14, v14, v42
	v_add_f32_e32 v15, v15, v43
	v_add_f32_e32 v16, v16, v44
	v_add_f32_e32 v10, v10, v42
	v_add_f32_e32 v11, v11, v43
	v_add_f32_e32 v12, v12, v44
	v_add_f32_e32 v2, v2, v42
	v_add_f32_e32 v3, v3, v43
	v_add_f32_e32 v4, v4, v44
	v_lshrrev_b32_e32 v18, 3, v18
	v_max_f32_e32 v14, 0, v14
	v_max_f32_e32 v15, 0, v15
	v_max_f32_e32 v16, 0, v16
	v_add_f32_e32 v17, v17, v45
	v_max_f32_e32 v10, 0, v10
	v_max_f32_e32 v11, 0, v11
	v_max_f32_e32 v12, 0, v12
	v_add_f32_e32 v13, v13, v45
	v_max_f32_e32 v2, 0, v2
	v_max_f32_e32 v3, 0, v3
	v_max_f32_e32 v4, 0, v4
	v_add_f32_e32 v5, v5, v45
	v_max_f32_e32 v17, 0, v17
	v_cvt_pk_bf16_f32 v14, v14, v15
	v_cvt_pk_bf16_f32 v15, v16, v17
	v_xor_b32_e32 v16, v18, v118
	v_max_f32_e32 v13, 0, v13
	v_cvt_pk_bf16_f32 v10, v10, v11
	v_cvt_pk_bf16_f32 v11, v12, v13
	v_bitop3_b32 v12, v18, v70, 31 bitop3:0x78
	v_max_f32_e32 v5, 0, v5
	v_cvt_pk_bf16_f32 v2, v2, v3
	v_cvt_pk_bf16_f32 v3, v4, v5
	v_bitop3_b32 v4, v18, v71, 31 bitop3:0x78
	v_lshlrev_b32_e32 v16, 4, v16
	v_lshlrev_b32_e32 v12, 4, v12
	v_add_f32_e32 v6, v6, v42
	v_add_f32_e32 v7, v7, v43
	v_lshlrev_b32_e32 v4, 4, v4
	v_add3_u32 v16, v69, v16, v68
	v_add3_u32 v12, v72, v12, v68
	v_max_f32_e32 v6, 0, v6
	v_max_f32_e32 v7, 0, v7
	v_add_f32_e32 v8, v8, v44
	v_add_f32_e32 v9, v9, v45
	v_add3_u32 v4, v73, v4, v68
	ds_write_b64 v16, v[14:15]
	ds_write_b64 v12, v[10:11]
	v_max_f32_e32 v8, 0, v8
	v_max_f32_e32 v9, 0, v9
	v_cvt_pk_bf16_f32 v6, v6, v7
	v_cvt_pk_bf16_f32 v7, v8, v9
	ds_write_b64 v16, v[6:7] offset:16384
	ds_write_b64 v4, v[2:3]
	v_and_b32_e32 v2, 0x1f0, v1
	v_mov_b32_e32 v3, 0
	v_lshl_add_u64 v[2:3], s[0:1], 0, v[2:3]
	s_mov_b64 s[0:1], 0x2000000
	v_ashrrev_i32_e32 v6, 5, v0
	v_lshl_add_u64 v[10:11], v[2:3], 0, s[0:1]
	v_xor_b32_e32 v2, v6, v0
	v_lshlrev_b32_e32 v2, 4, v2
	v_lshlrev_b32_e32 v1, 9, v6
	v_and_b32_e32 v2, 0x1f0, v2
	v_add3_u32 v1, 0, v1, v2
	s_waitcnt lgkmcnt(0)
	s_barrier
	ds_read_b128 v[2:5], v1
	v_ashrrev_i32_e32 v7, 31, v6
	v_add_u32_e32 v1, 0x200, v0
	v_lshlrev_b64 v[6:7], 11, v[6:7]
	v_ashrrev_i32_e32 v14, 5, v1
	v_lshl_add_u64 v[12:13], v[10:11], 0, v[6:7]
	v_xor_b32_e32 v6, v14, v0
	v_lshlrev_b32_e32 v6, 4, v6
	v_lshlrev_b32_e32 v1, 9, v14
	v_and_b32_e32 v6, 0x1f0, v6
	v_add3_u32 v1, 0, v1, v6
	ds_read_b128 v[6:9], v1
	v_ashrrev_i32_e32 v15, 31, v14
	s_waitcnt lgkmcnt(1)
	global_store_dwordx4 v[12:13], v[2:5], off sc1
	v_add_u32_e32 v1, 0x400, v0
	s_nop 0
	v_lshlrev_b64 v[2:3], 11, v[14:15]
	v_lshl_add_u64 v[2:3], v[10:11], 0, v[2:3]
	s_waitcnt lgkmcnt(0)
	global_store_dwordx4 v[2:3], v[6:9], off sc1
	s_nop 1
	v_ashrrev_i32_e32 v6, 5, v1
	v_xor_b32_e32 v2, v6, v0
	v_lshlrev_b32_e32 v2, 4, v2
	v_lshlrev_b32_e32 v1, 9, v6
	v_and_b32_e32 v2, 0x1f0, v2
	v_add3_u32 v1, 0, v1, v2
	ds_read_b128 v[2:5], v1
	v_ashrrev_i32_e32 v7, 31, v6
	v_add_u32_e32 v1, 0x600, v0
	v_lshlrev_b64 v[6:7], 11, v[6:7]
	v_ashrrev_i32_e32 v14, 5, v1
	v_lshl_add_u64 v[12:13], v[10:11], 0, v[6:7]
	v_xor_b32_e32 v6, v14, v0
	v_lshlrev_b32_e32 v6, 4, v6
	v_lshlrev_b32_e32 v1, 9, v14
	v_and_b32_e32 v6, 0x1f0, v6
	v_add3_u32 v1, 0, v1, v6
	ds_read_b128 v[6:9], v1
	v_ashrrev_i32_e32 v15, 31, v14
	s_waitcnt lgkmcnt(1)
	global_store_dwordx4 v[12:13], v[2:5], off sc1
	v_add_u32_e32 v1, 0x800, v0
	s_nop 0
	v_lshlrev_b64 v[2:3], 11, v[14:15]
	v_lshl_add_u64 v[2:3], v[10:11], 0, v[2:3]
	s_waitcnt lgkmcnt(0)
	global_store_dwordx4 v[2:3], v[6:9], off sc1
	s_nop 1
	v_ashrrev_i32_e32 v6, 5, v1
	v_xor_b32_e32 v2, v6, v0
	v_lshlrev_b32_e32 v2, 4, v2
	v_lshlrev_b32_e32 v1, 9, v6
	v_and_b32_e32 v2, 0x1f0, v2
	v_add3_u32 v1, 0, v1, v2
	ds_read_b128 v[2:5], v1
	v_ashrrev_i32_e32 v7, 31, v6
	v_add_u32_e32 v1, 0xa00, v0
	v_lshlrev_b64 v[6:7], 11, v[6:7]
	v_ashrrev_i32_e32 v14, 5, v1
	v_lshl_add_u64 v[12:13], v[10:11], 0, v[6:7]
	v_xor_b32_e32 v6, v14, v0
	v_lshlrev_b32_e32 v6, 4, v6
	v_lshlrev_b32_e32 v1, 9, v14
	v_and_b32_e32 v6, 0x1f0, v6
	v_add3_u32 v1, 0, v1, v6
	ds_read_b128 v[6:9], v1
	v_ashrrev_i32_e32 v15, 31, v14
	s_waitcnt lgkmcnt(1)
	global_store_dwordx4 v[12:13], v[2:5], off sc1
	v_add_u32_e32 v1, 0xc00, v0
	s_nop 0
	v_lshlrev_b64 v[2:3], 11, v[14:15]
	v_lshl_add_u64 v[2:3], v[10:11], 0, v[2:3]
	s_waitcnt lgkmcnt(0)
	global_store_dwordx4 v[2:3], v[6:9], off sc1
	s_nop 1
	v_ashrrev_i32_e32 v6, 5, v1
	v_xor_b32_e32 v2, v6, v0
	v_lshlrev_b32_e32 v2, 4, v2
	v_lshlrev_b32_e32 v1, 9, v6
	v_and_b32_e32 v2, 0x1f0, v2
	v_add3_u32 v1, 0, v1, v2
	ds_read_b128 v[2:5], v1
	v_add_u32_e32 v1, 0xe00, v0
	v_ashrrev_i32_e32 v14, 5, v1
	v_xor_b32_e32 v0, v14, v0
	v_lshlrev_b32_e32 v0, 4, v0
	v_ashrrev_i32_e32 v7, 31, v6
	v_lshlrev_b32_e32 v1, 9, v14
	v_and_b32_e32 v0, 0x1f0, v0
	v_lshlrev_b64 v[6:7], 11, v[6:7]
	v_add3_u32 v0, 0, v1, v0
	v_lshl_add_u64 v[12:13], v[10:11], 0, v[6:7]
	ds_read_b128 v[6:9], v0
	v_ashrrev_i32_e32 v15, 31, v14
	v_lshlrev_b64 v[0:1], 11, v[14:15]
	v_lshl_add_u64 v[0:1], v[10:11], 0, v[0:1]
	s_waitcnt lgkmcnt(1)
	global_store_dwordx4 v[12:13], v[2:5], off sc1
	s_waitcnt lgkmcnt(0)
	global_store_dwordx4 v[0:1], v[6:9], off sc1
	s_endpgm
